# DPP cumulative-sum blocks: counted vmcnt waits staged in load-arrival order (was one vmcnt(0))
# baseline (speedup 1.0000x reference)
.LBB0_361:
	s_ashr_i32 s14, s18, 2
	s_ashr_i32 s15, s14, 31
	s_lshl_b64 s[30:31], s[14:15], 15
	v_mov_b32_e32 v13, s31
	v_or_b32_e32 v12, s30, v34
	v_lshl_add_u64 v[30:31], s[26:27], 0, v[12:13]
	global_load_dwordx4 v[14:17], v[30:31], off
	global_load_dwordx4 v[18:21], v[30:31], off offset:16
	global_load_dwordx4 v[22:25], v[30:31], off offset:32
	global_load_dwordx4 v[26:29], v[30:31], off offset:48
	s_waitcnt lgkmcnt(0)
	global_load_dwordx4 v[0:3], v[30:31], off offset:112
	global_load_dwordx4 v[4:7], v[30:31], off offset:96
	global_load_dwordx4 v[8:11], v[30:31], off offset:80
	global_load_dwordx4 v[76:79], v[30:31], off offset:64
	s_waitcnt vmcnt(6)
	s_nop 1
	v_add_f32_dpp v14, v14, v14 row_shr:1 row_mask:0xf bank_mask:0xf bound_ctrl:0
	v_add_f32_dpp v15, v15, v15 row_shr:1 row_mask:0xf bank_mask:0xf bound_ctrl:0
	v_add_f32_dpp v16, v16, v16 row_shr:1 row_mask:0xf bank_mask:0xf bound_ctrl:0
	v_add_f32_dpp v17, v17, v17 row_shr:1 row_mask:0xf bank_mask:0xf bound_ctrl:0
	v_add_f32_dpp v18, v18, v18 row_shr:1 row_mask:0xf bank_mask:0xf bound_ctrl:0
	v_add_f32_dpp v19, v19, v19 row_shr:1 row_mask:0xf bank_mask:0xf bound_ctrl:0
	v_add_f32_dpp v20, v20, v20 row_shr:1 row_mask:0xf bank_mask:0xf bound_ctrl:0
	v_add_f32_dpp v21, v21, v21 row_shr:1 row_mask:0xf bank_mask:0xf bound_ctrl:0
	v_add_f32_dpp v14, v14, v14 row_shr:2 row_mask:0xf bank_mask:0xf bound_ctrl:0
	v_add_f32_dpp v15, v15, v15 row_shr:2 row_mask:0xf bank_mask:0xf bound_ctrl:0
	v_add_f32_dpp v16, v16, v16 row_shr:2 row_mask:0xf bank_mask:0xf bound_ctrl:0
	v_add_f32_dpp v17, v17, v17 row_shr:2 row_mask:0xf bank_mask:0xf bound_ctrl:0
	v_add_f32_dpp v18, v18, v18 row_shr:2 row_mask:0xf bank_mask:0xf bound_ctrl:0
	v_add_f32_dpp v19, v19, v19 row_shr:2 row_mask:0xf bank_mask:0xf bound_ctrl:0
	v_add_f32_dpp v20, v20, v20 row_shr:2 row_mask:0xf bank_mask:0xf bound_ctrl:0
	v_add_f32_dpp v21, v21, v21 row_shr:2 row_mask:0xf bank_mask:0xf bound_ctrl:0
	v_add_f32_dpp v14, v14, v14 row_shr:4 row_mask:0xf bank_mask:0xf bound_ctrl:0
	v_add_f32_dpp v15, v15, v15 row_shr:4 row_mask:0xf bank_mask:0xf bound_ctrl:0
	v_add_f32_dpp v16, v16, v16 row_shr:4 row_mask:0xf bank_mask:0xf bound_ctrl:0
	v_add_f32_dpp v17, v17, v17 row_shr:4 row_mask:0xf bank_mask:0xf bound_ctrl:0
	v_add_f32_dpp v18, v18, v18 row_shr:4 row_mask:0xf bank_mask:0xf bound_ctrl:0
	v_add_f32_dpp v19, v19, v19 row_shr:4 row_mask:0xf bank_mask:0xf bound_ctrl:0
	v_add_f32_dpp v20, v20, v20 row_shr:4 row_mask:0xf bank_mask:0xf bound_ctrl:0
	v_add_f32_dpp v21, v21, v21 row_shr:4 row_mask:0xf bank_mask:0xf bound_ctrl:0
	v_add_f32_dpp v14, v14, v14 row_shr:8 row_mask:0xf bank_mask:0xf bound_ctrl:0
	v_add_f32_dpp v15, v15, v15 row_shr:8 row_mask:0xf bank_mask:0xf bound_ctrl:0
	v_add_f32_dpp v16, v16, v16 row_shr:8 row_mask:0xf bank_mask:0xf bound_ctrl:0
	v_add_f32_dpp v17, v17, v17 row_shr:8 row_mask:0xf bank_mask:0xf bound_ctrl:0
	v_add_f32_dpp v18, v18, v18 row_shr:8 row_mask:0xf bank_mask:0xf bound_ctrl:0
	v_add_f32_dpp v19, v19, v19 row_shr:8 row_mask:0xf bank_mask:0xf bound_ctrl:0
	v_add_f32_dpp v20, v20, v20 row_shr:8 row_mask:0xf bank_mask:0xf bound_ctrl:0
	v_add_f32_dpp v21, v21, v21 row_shr:8 row_mask:0xf bank_mask:0xf bound_ctrl:0
	v_add_f32_dpp v14, v14, v14 row_bcast:15 row_mask:0xa bank_mask:0xf
	v_add_f32_dpp v15, v15, v15 row_bcast:15 row_mask:0xa bank_mask:0xf
	v_add_f32_dpp v16, v16, v16 row_bcast:15 row_mask:0xa bank_mask:0xf
	v_add_f32_dpp v17, v17, v17 row_bcast:15 row_mask:0xa bank_mask:0xf
	v_add_f32_dpp v18, v18, v18 row_bcast:15 row_mask:0xa bank_mask:0xf
	v_add_f32_dpp v19, v19, v19 row_bcast:15 row_mask:0xa bank_mask:0xf
	v_add_f32_dpp v20, v20, v20 row_bcast:15 row_mask:0xa bank_mask:0xf
	v_add_f32_dpp v21, v21, v21 row_bcast:15 row_mask:0xa bank_mask:0xf
	v_add_f32_dpp v14, v14, v14 row_bcast:31 row_mask:0xc bank_mask:0xf
	v_add_f32_dpp v15, v15, v15 row_bcast:31 row_mask:0xc bank_mask:0xf
	v_add_f32_dpp v16, v16, v16 row_bcast:31 row_mask:0xc bank_mask:0xf
	v_add_f32_dpp v17, v17, v17 row_bcast:31 row_mask:0xc bank_mask:0xf
	v_add_f32_dpp v18, v18, v18 row_bcast:31 row_mask:0xc bank_mask:0xf
	v_add_f32_dpp v19, v19, v19 row_bcast:31 row_mask:0xc bank_mask:0xf
	v_add_f32_dpp v20, v20, v20 row_bcast:31 row_mask:0xc bank_mask:0xf
	v_add_f32_dpp v21, v21, v21 row_bcast:31 row_mask:0xc bank_mask:0xf
	s_waitcnt vmcnt(4)
	s_nop 1
	v_add_f32_dpp v22, v22, v22 row_shr:1 row_mask:0xf bank_mask:0xf bound_ctrl:0
	v_add_f32_dpp v23, v23, v23 row_shr:1 row_mask:0xf bank_mask:0xf bound_ctrl:0
	v_add_f32_dpp v24, v24, v24 row_shr:1 row_mask:0xf bank_mask:0xf bound_ctrl:0
	v_add_f32_dpp v25, v25, v25 row_shr:1 row_mask:0xf bank_mask:0xf bound_ctrl:0
	v_add_f32_dpp v26, v26, v26 row_shr:1 row_mask:0xf bank_mask:0xf bound_ctrl:0
	v_add_f32_dpp v27, v27, v27 row_shr:1 row_mask:0xf bank_mask:0xf bound_ctrl:0
	v_add_f32_dpp v28, v28, v28 row_shr:1 row_mask:0xf bank_mask:0xf bound_ctrl:0
	v_add_f32_dpp v29, v29, v29 row_shr:1 row_mask:0xf bank_mask:0xf bound_ctrl:0
	v_add_f32_dpp v22, v22, v22 row_shr:2 row_mask:0xf bank_mask:0xf bound_ctrl:0
	v_add_f32_dpp v23, v23, v23 row_shr:2 row_mask:0xf bank_mask:0xf bound_ctrl:0
	v_add_f32_dpp v24, v24, v24 row_shr:2 row_mask:0xf bank_mask:0xf bound_ctrl:0
	v_add_f32_dpp v25, v25, v25 row_shr:2 row_mask:0xf bank_mask:0xf bound_ctrl:0
	v_add_f32_dpp v26, v26, v26 row_shr:2 row_mask:0xf bank_mask:0xf bound_ctrl:0
	v_add_f32_dpp v27, v27, v27 row_shr:2 row_mask:0xf bank_mask:0xf bound_ctrl:0
	v_add_f32_dpp v28, v28, v28 row_shr:2 row_mask:0xf bank_mask:0xf bound_ctrl:0
	v_add_f32_dpp v29, v29, v29 row_shr:2 row_mask:0xf bank_mask:0xf bound_ctrl:0
	v_add_f32_dpp v22, v22, v22 row_shr:4 row_mask:0xf bank_mask:0xf bound_ctrl:0
	v_add_f32_dpp v23, v23, v23 row_shr:4 row_mask:0xf bank_mask:0xf bound_ctrl:0
	v_add_f32_dpp v24, v24, v24 row_shr:4 row_mask:0xf bank_mask:0xf bound_ctrl:0
	v_add_f32_dpp v25, v25, v25 row_shr:4 row_mask:0xf bank_mask:0xf bound_ctrl:0
	v_add_f32_dpp v26, v26, v26 row_shr:4 row_mask:0xf bank_mask:0xf bound_ctrl:0
	v_add_f32_dpp v27, v27, v27 row_shr:4 row_mask:0xf bank_mask:0xf bound_ctrl:0
	v_add_f32_dpp v28, v28, v28 row_shr:4 row_mask:0xf bank_mask:0xf bound_ctrl:0
	v_add_f32_dpp v29, v29, v29 row_shr:4 row_mask:0xf bank_mask:0xf bound_ctrl:0
	v_add_f32_dpp v22, v22, v22 row_shr:8 row_mask:0xf bank_mask:0xf bound_ctrl:0
	v_add_f32_dpp v23, v23, v23 row_shr:8 row_mask:0xf bank_mask:0xf bound_ctrl:0
	v_add_f32_dpp v24, v24, v24 row_shr:8 row_mask:0xf bank_mask:0xf bound_ctrl:0
	v_add_f32_dpp v25, v25, v25 row_shr:8 row_mask:0xf bank_mask:0xf bound_ctrl:0
	v_add_f32_dpp v26, v26, v26 row_shr:8 row_mask:0xf bank_mask:0xf bound_ctrl:0
	v_add_f32_dpp v27, v27, v27 row_shr:8 row_mask:0xf bank_mask:0xf bound_ctrl:0
	v_add_f32_dpp v28, v28, v28 row_shr:8 row_mask:0xf bank_mask:0xf bound_ctrl:0
	v_add_f32_dpp v29, v29, v29 row_shr:8 row_mask:0xf bank_mask:0xf bound_ctrl:0
	v_add_f32_dpp v22, v22, v22 row_bcast:15 row_mask:0xa bank_mask:0xf
	v_add_f32_dpp v23, v23, v23 row_bcast:15 row_mask:0xa bank_mask:0xf
	v_add_f32_dpp v24, v24, v24 row_bcast:15 row_mask:0xa bank_mask:0xf
	v_add_f32_dpp v25, v25, v25 row_bcast:15 row_mask:0xa bank_mask:0xf
	v_add_f32_dpp v26, v26, v26 row_bcast:15 row_mask:0xa bank_mask:0xf
	v_add_f32_dpp v27, v27, v27 row_bcast:15 row_mask:0xa bank_mask:0xf
	v_add_f32_dpp v28, v28, v28 row_bcast:15 row_mask:0xa bank_mask:0xf
	v_add_f32_dpp v29, v29, v29 row_bcast:15 row_mask:0xa bank_mask:0xf
	v_add_f32_dpp v22, v22, v22 row_bcast:31 row_mask:0xc bank_mask:0xf
	v_add_f32_dpp v23, v23, v23 row_bcast:31 row_mask:0xc bank_mask:0xf
	v_add_f32_dpp v24, v24, v24 row_bcast:31 row_mask:0xc bank_mask:0xf
	v_add_f32_dpp v25, v25, v25 row_bcast:31 row_mask:0xc bank_mask:0xf
	v_add_f32_dpp v26, v26, v26 row_bcast:31 row_mask:0xc bank_mask:0xf
	v_add_f32_dpp v27, v27, v27 row_bcast:31 row_mask:0xc bank_mask:0xf
	v_add_f32_dpp v28, v28, v28 row_bcast:31 row_mask:0xc bank_mask:0xf
	v_add_f32_dpp v29, v29, v29 row_bcast:31 row_mask:0xc bank_mask:0xf
	s_waitcnt vmcnt(2)
	s_nop 1
	v_add_f32_dpp v4, v4, v4 row_shr:1 row_mask:0xf bank_mask:0xf bound_ctrl:0
	v_add_f32_dpp v5, v5, v5 row_shr:1 row_mask:0xf bank_mask:0xf bound_ctrl:0
	v_add_f32_dpp v6, v6, v6 row_shr:1 row_mask:0xf bank_mask:0xf bound_ctrl:0
	v_add_f32_dpp v7, v7, v7 row_shr:1 row_mask:0xf bank_mask:0xf bound_ctrl:0
	v_add_f32_dpp v0, v0, v0 row_shr:1 row_mask:0xf bank_mask:0xf bound_ctrl:0
	v_add_f32_dpp v1, v1, v1 row_shr:1 row_mask:0xf bank_mask:0xf bound_ctrl:0
	v_add_f32_dpp v2, v2, v2 row_shr:1 row_mask:0xf bank_mask:0xf bound_ctrl:0
	v_add_f32_dpp v3, v3, v3 row_shr:1 row_mask:0xf bank_mask:0xf bound_ctrl:0
	v_add_f32_dpp v4, v4, v4 row_shr:2 row_mask:0xf bank_mask:0xf bound_ctrl:0
	v_add_f32_dpp v5, v5, v5 row_shr:2 row_mask:0xf bank_mask:0xf bound_ctrl:0
	v_add_f32_dpp v6, v6, v6 row_shr:2 row_mask:0xf bank_mask:0xf bound_ctrl:0
	v_add_f32_dpp v7, v7, v7 row_shr:2 row_mask:0xf bank_mask:0xf bound_ctrl:0
	v_add_f32_dpp v0, v0, v0 row_shr:2 row_mask:0xf bank_mask:0xf bound_ctrl:0
	v_add_f32_dpp v1, v1, v1 row_shr:2 row_mask:0xf bank_mask:0xf bound_ctrl:0
	v_add_f32_dpp v2, v2, v2 row_shr:2 row_mask:0xf bank_mask:0xf bound_ctrl:0
	v_add_f32_dpp v3, v3, v3 row_shr:2 row_mask:0xf bank_mask:0xf bound_ctrl:0
	v_add_f32_dpp v4, v4, v4 row_shr:4 row_mask:0xf bank_mask:0xf bound_ctrl:0
	v_add_f32_dpp v5, v5, v5 row_shr:4 row_mask:0xf bank_mask:0xf bound_ctrl:0
	v_add_f32_dpp v6, v6, v6 row_shr:4 row_mask:0xf bank_mask:0xf bound_ctrl:0
	v_add_f32_dpp v7, v7, v7 row_shr:4 row_mask:0xf bank_mask:0xf bound_ctrl:0
	v_add_f32_dpp v0, v0, v0 row_shr:4 row_mask:0xf bank_mask:0xf bound_ctrl:0
	v_add_f32_dpp v1, v1, v1 row_shr:4 row_mask:0xf bank_mask:0xf bound_ctrl:0
	v_add_f32_dpp v2, v2, v2 row_shr:4 row_mask:0xf bank_mask:0xf bound_ctrl:0
	v_add_f32_dpp v3, v3, v3 row_shr:4 row_mask:0xf bank_mask:0xf bound_ctrl:0
	v_add_f32_dpp v4, v4, v4 row_shr:8 row_mask:0xf bank_mask:0xf bound_ctrl:0
	v_add_f32_dpp v5, v5, v5 row_shr:8 row_mask:0xf bank_mask:0xf bound_ctrl:0
	v_add_f32_dpp v6, v6, v6 row_shr:8 row_mask:0xf bank_mask:0xf bound_ctrl:0
	v_add_f32_dpp v7, v7, v7 row_shr:8 row_mask:0xf bank_mask:0xf bound_ctrl:0
	v_add_f32_dpp v0, v0, v0 row_shr:8 row_mask:0xf bank_mask:0xf bound_ctrl:0
	v_add_f32_dpp v1, v1, v1 row_shr:8 row_mask:0xf bank_mask:0xf bound_ctrl:0
	v_add_f32_dpp v2, v2, v2 row_shr:8 row_mask:0xf bank_mask:0xf bound_ctrl:0
	v_add_f32_dpp v3, v3, v3 row_shr:8 row_mask:0xf bank_mask:0xf bound_ctrl:0
	v_add_f32_dpp v4, v4, v4 row_bcast:15 row_mask:0xa bank_mask:0xf
	v_add_f32_dpp v5, v5, v5 row_bcast:15 row_mask:0xa bank_mask:0xf
	v_add_f32_dpp v6, v6, v6 row_bcast:15 row_mask:0xa bank_mask:0xf
	v_add_f32_dpp v7, v7, v7 row_bcast:15 row_mask:0xa bank_mask:0xf
	v_add_f32_dpp v0, v0, v0 row_bcast:15 row_mask:0xa bank_mask:0xf
	v_add_f32_dpp v1, v1, v1 row_bcast:15 row_mask:0xa bank_mask:0xf
	v_add_f32_dpp v2, v2, v2 row_bcast:15 row_mask:0xa bank_mask:0xf
	v_add_f32_dpp v3, v3, v3 row_bcast:15 row_mask:0xa bank_mask:0xf
	v_add_f32_dpp v4, v4, v4 row_bcast:31 row_mask:0xc bank_mask:0xf
	v_add_f32_dpp v5, v5, v5 row_bcast:31 row_mask:0xc bank_mask:0xf
	v_add_f32_dpp v6, v6, v6 row_bcast:31 row_mask:0xc bank_mask:0xf
	v_add_f32_dpp v7, v7, v7 row_bcast:31 row_mask:0xc bank_mask:0xf
	v_add_f32_dpp v0, v0, v0 row_bcast:31 row_mask:0xc bank_mask:0xf
	v_add_f32_dpp v1, v1, v1 row_bcast:31 row_mask:0xc bank_mask:0xf
	v_add_f32_dpp v2, v2, v2 row_bcast:31 row_mask:0xc bank_mask:0xf
	v_add_f32_dpp v3, v3, v3 row_bcast:31 row_mask:0xc bank_mask:0xf
	s_waitcnt vmcnt(0)
	s_nop 1
	v_add_f32_dpp v76, v76, v76 row_shr:1 row_mask:0xf bank_mask:0xf bound_ctrl:0
	v_add_f32_dpp v77, v77, v77 row_shr:1 row_mask:0xf bank_mask:0xf bound_ctrl:0
	v_add_f32_dpp v78, v78, v78 row_shr:1 row_mask:0xf bank_mask:0xf bound_ctrl:0
	v_add_f32_dpp v79, v79, v79 row_shr:1 row_mask:0xf bank_mask:0xf bound_ctrl:0
	v_add_f32_dpp v8, v8, v8 row_shr:1 row_mask:0xf bank_mask:0xf bound_ctrl:0
	v_add_f32_dpp v9, v9, v9 row_shr:1 row_mask:0xf bank_mask:0xf bound_ctrl:0
	v_add_f32_dpp v10, v10, v10 row_shr:1 row_mask:0xf bank_mask:0xf bound_ctrl:0
	v_add_f32_dpp v11, v11, v11 row_shr:1 row_mask:0xf bank_mask:0xf bound_ctrl:0
	v_add_f32_dpp v76, v76, v76 row_shr:2 row_mask:0xf bank_mask:0xf bound_ctrl:0
	v_add_f32_dpp v77, v77, v77 row_shr:2 row_mask:0xf bank_mask:0xf bound_ctrl:0
	v_add_f32_dpp v78, v78, v78 row_shr:2 row_mask:0xf bank_mask:0xf bound_ctrl:0
	v_add_f32_dpp v79, v79, v79 row_shr:2 row_mask:0xf bank_mask:0xf bound_ctrl:0
	v_add_f32_dpp v8, v8, v8 row_shr:2 row_mask:0xf bank_mask:0xf bound_ctrl:0
	v_add_f32_dpp v9, v9, v9 row_shr:2 row_mask:0xf bank_mask:0xf bound_ctrl:0
	v_add_f32_dpp v10, v10, v10 row_shr:2 row_mask:0xf bank_mask:0xf bound_ctrl:0
	v_add_f32_dpp v11, v11, v11 row_shr:2 row_mask:0xf bank_mask:0xf bound_ctrl:0
	v_add_f32_dpp v76, v76, v76 row_shr:4 row_mask:0xf bank_mask:0xf bound_ctrl:0
	v_add_f32_dpp v77, v77, v77 row_shr:4 row_mask:0xf bank_mask:0xf bound_ctrl:0
	v_add_f32_dpp v78, v78, v78 row_shr:4 row_mask:0xf bank_mask:0xf bound_ctrl:0
	v_add_f32_dpp v79, v79, v79 row_shr:4 row_mask:0xf bank_mask:0xf bound_ctrl:0
	v_add_f32_dpp v8, v8, v8 row_shr:4 row_mask:0xf bank_mask:0xf bound_ctrl:0
	v_add_f32_dpp v9, v9, v9 row_shr:4 row_mask:0xf bank_mask:0xf bound_ctrl:0
	v_add_f32_dpp v10, v10, v10 row_shr:4 row_mask:0xf bank_mask:0xf bound_ctrl:0
	v_add_f32_dpp v11, v11, v11 row_shr:4 row_mask:0xf bank_mask:0xf bound_ctrl:0
	v_add_f32_dpp v76, v76, v76 row_shr:8 row_mask:0xf bank_mask:0xf bound_ctrl:0
	v_add_f32_dpp v77, v77, v77 row_shr:8 row_mask:0xf bank_mask:0xf bound_ctrl:0
	v_add_f32_dpp v78, v78, v78 row_shr:8 row_mask:0xf bank_mask:0xf bound_ctrl:0
	v_add_f32_dpp v79, v79, v79 row_shr:8 row_mask:0xf bank_mask:0xf bound_ctrl:0
	v_add_f32_dpp v8, v8, v8 row_shr:8 row_mask:0xf bank_mask:0xf bound_ctrl:0
	v_add_f32_dpp v9, v9, v9 row_shr:8 row_mask:0xf bank_mask:0xf bound_ctrl:0
	v_add_f32_dpp v10, v10, v10 row_shr:8 row_mask:0xf bank_mask:0xf bound_ctrl:0
	v_add_f32_dpp v11, v11, v11 row_shr:8 row_mask:0xf bank_mask:0xf bound_ctrl:0
	v_add_f32_dpp v76, v76, v76 row_bcast:15 row_mask:0xa bank_mask:0xf
	v_add_f32_dpp v77, v77, v77 row_bcast:15 row_mask:0xa bank_mask:0xf
	v_add_f32_dpp v78, v78, v78 row_bcast:15 row_mask:0xa bank_mask:0xf
	v_add_f32_dpp v79, v79, v79 row_bcast:15 row_mask:0xa bank_mask:0xf
	v_add_f32_dpp v8, v8, v8 row_bcast:15 row_mask:0xa bank_mask:0xf
	v_add_f32_dpp v9, v9, v9 row_bcast:15 row_mask:0xa bank_mask:0xf
	v_add_f32_dpp v10, v10, v10 row_bcast:15 row_mask:0xa bank_mask:0xf
	v_add_f32_dpp v11, v11, v11 row_bcast:15 row_mask:0xa bank_mask:0xf
	v_add_f32_dpp v76, v76, v76 row_bcast:31 row_mask:0xc bank_mask:0xf
	v_add_f32_dpp v77, v77, v77 row_bcast:31 row_mask:0xc bank_mask:0xf
	v_add_f32_dpp v78, v78, v78 row_bcast:31 row_mask:0xc bank_mask:0xf
	v_add_f32_dpp v79, v79, v79 row_bcast:31 row_mask:0xc bank_mask:0xf
	v_add_f32_dpp v8, v8, v8 row_bcast:31 row_mask:0xc bank_mask:0xf
	v_add_f32_dpp v9, v9, v9 row_bcast:31 row_mask:0xc bank_mask:0xf
	v_add_f32_dpp v10, v10, v10 row_bcast:31 row_mask:0xc bank_mask:0xf
	v_add_f32_dpp v11, v11, v11 row_bcast:31 row_mask:0xc bank_mask:0xf
	v_mov_b32_e32 v90, v14
	v_mov_b32_e32 v91, v15
	v_mov_b32_e32 v92, v16
	v_mov_b32_e32 v93, v17
	v_mov_b32_e32 v30, v76
	v_mov_b32_e32 v31, v77
	v_mov_b32_e32 v81, v10
	v_mov_b32_e32 v82, v11
	v_mov_b32_e32 v80, v4
	v_mov_b32_e32 v83, v5
	v_mov_b32_e32 v84, v6
	v_mov_b32_e32 v85, v7
	v_mov_b32_e32 v86, v0
	v_mov_b32_e32 v87, v1
	v_mov_b32_e32 v88, v2
	v_mov_b32_e32 v89, v3
	v_mov_b32_e32 v76, v78
	v_mov_b32_e32 v77, v79
	v_mov_b32_e32 v78, v8
	v_mov_b32_e32 v79, v9
	s_nop 0
	s_mov_b32 s15, 0x3ab00000
	s_mov_b64 s[30:31], 0x3ab00100
	s_waitcnt lgkmcnt(0)
	s_nop 0
	v_readlane_b32 s19, v91, 63
	s_nop 0
	v_sub_f32_e32 v91, s19, v91
	s_waitcnt lgkmcnt(0)
	s_waitcnt lgkmcnt(0)
	v_mul_f32_e32 v91, 0x3fb8aa3b, v91
	v_exp_f32_e32 v91, v91
	v_readlane_b32 s48, v93, 63
	s_waitcnt lgkmcnt(0)
	s_nop 0
	v_readlane_b32 s50, v18, 63
	s_nop 0
	s_waitcnt lgkmcnt(0)
	s_waitcnt lgkmcnt(0)
	s_waitcnt lgkmcnt(0)
	v_readlane_b32 s49, v20, 63
	v_readlane_b32 s51, v21, 63
	s_nop 0
	s_waitcnt lgkmcnt(0)
	s_waitcnt lgkmcnt(0)
	v_readlane_b32 s52, v22, 63
	v_readlane_b32 s53, v23, 63
	s_waitcnt lgkmcnt(0)
	s_nop 0
	v_readlane_b32 s54, v24, 63
	s_nop 0
	s_waitcnt lgkmcnt(0)
	s_waitcnt lgkmcnt(0)
	v_readlane_b32 s56, v25, 63
	v_readlane_b32 s55, v26, 63
	s_waitcnt lgkmcnt(0)
	s_nop 0
	v_readlane_b32 s57, v27, 63
	s_nop 0
	s_waitcnt lgkmcnt(0)
	s_waitcnt lgkmcnt(0)
	v_readlane_b32 s58, v28, 63
	v_readlane_b32 s59, v29, 63
	s_waitcnt lgkmcnt(0)
	s_nop 0
	v_readlane_b32 s60, v30, 63
	s_nop 0
	s_waitcnt lgkmcnt(0)
	s_waitcnt lgkmcnt(0)
	v_readlane_b32 s61, v31, 63
	v_readlane_b32 s62, v76, 63
	s_waitcnt lgkmcnt(0)
	s_nop 0
	v_readlane_b32 s63, v77, 63
	s_nop 0
	s_nop 0
	s_nop 1
	v_lshl_add_u64 v[0:1], s[20:21], 0, v[12:13]
	v_lshl_add_u64 v[4:5], v[0:1], 0, s[86:87]
	v_add_co_u32_e32 v0, vcc, s15, v4
	s_nop 0
	v_addc_co_u32_e32 v1, vcc, 0, v5, vcc
	global_load_dwordx4 v[0:3], v[0:1], off offset:256
	v_lshl_add_u64 v[14:15], v[4:5], 0, s[30:31]
	s_waitcnt lgkmcnt(1)
	global_load_dwordx4 v[4:7], v[14:15], off offset:32
	global_load_dwordx4 v[8:11], v[14:15], off offset:16
	s_waitcnt lgkmcnt(1)
	s_waitcnt lgkmcnt(0)
	v_readlane_b32 s15, v90, 63
	v_sub_f32_e32 v90, s15, v90
	s_waitcnt lgkmcnt(1)
	v_mul_f32_e32 v90, 0x3fb8aa3b, v90
	s_waitcnt lgkmcnt(0)
	v_exp_f32_e32 v90, v90
	s_waitcnt lgkmcnt(1)
	s_waitcnt lgkmcnt(1)
	s_waitcnt lgkmcnt(0)
	global_load_dwordx4 v[14:17], v[14:15], off offset:48
	s_waitcnt lgkmcnt(1)
	s_waitcnt lgkmcnt(1)
	v_readlane_b32 vcc_hi, v92, 63
	s_waitcnt lgkmcnt(0)
	s_waitcnt vmcnt(3)
	v_lshlrev_b32_e32 v94, 16, v0
	v_and_b32_e32 v0, 0xffff0000, v0
	v_mul_f32_e32 v0, v91, v0
	v_cvt_pk_bf16_f32 v0, v0, s0
	v_mul_f32_e32 v90, v90, v94
	ds_write_b16 v54, v0 offset:128
	v_sub_f32_e32 v0, vcc_hi, v92
	v_cvt_pk_bf16_f32 v90, v90, s0
	v_mul_f32_e32 v0, 0x3fb8aa3b, v0
	ds_write_b16 v54, v90
	v_exp_f32_e32 v0, v0
	v_sub_f32_e32 v90, s48, v93
	v_mul_f32_e32 v90, 0x3fb8aa3b, v90
	v_exp_f32_e32 v90, v90
	v_lshlrev_b32_e32 v95, 16, v1
	v_mul_f32_e32 v0, v0, v95
	v_and_b32_e32 v1, 0xffff0000, v1
	v_cvt_pk_bf16_f32 v0, v0, s0
	ds_write_b16 v54, v0 offset:256
	v_mul_f32_e32 v0, v90, v1
	v_cvt_pk_bf16_f32 v0, v0, s0
	ds_write_b16 v54, v0 offset:384
	v_sub_f32_e32 v0, s50, v18
	v_mul_f32_e32 v0, 0x3fb8aa3b, v0
	v_readlane_b32 vcc_lo, v19, 63
	v_exp_f32_e32 v0, v0
	v_lshlrev_b32_e32 v96, 16, v2
	v_sub_f32_e32 v1, vcc_lo, v19
	v_mul_f32_e32 v1, 0x3fb8aa3b, v1
	v_exp_f32_e32 v1, v1
	v_mul_f32_e32 v0, v0, v96
	v_and_b32_e32 v2, 0xffff0000, v2
	v_cvt_pk_bf16_f32 v0, v0, s0
	ds_write_b16 v54, v0 offset:512
	v_mul_f32_e32 v0, v1, v2
	v_cvt_pk_bf16_f32 v0, v0, s0
	ds_write_b16 v54, v0 offset:640
	v_sub_f32_e32 v0, s49, v20
	v_mul_f32_e32 v0, 0x3fb8aa3b, v0
	v_exp_f32_e32 v0, v0
	v_sub_f32_e32 v1, s51, v21
	v_mul_f32_e32 v1, 0x3fb8aa3b, v1
	v_exp_f32_e32 v1, v1
	v_lshlrev_b32_e32 v98, 16, v3
	v_mul_f32_e32 v0, v0, v98
	v_and_b32_e32 v3, 0xffff0000, v3
	v_cvt_pk_bf16_f32 v0, v0, s0
	ds_write_b16 v54, v0 offset:768
	v_mul_f32_e32 v0, v1, v3
	v_cvt_pk_bf16_f32 v0, v0, s0
	ds_write_b16 v54, v0 offset:896
	v_sub_f32_e32 v0, s52, v22
	v_mul_f32_e32 v0, 0x3fb8aa3b, v0
	v_exp_f32_e32 v0, v0
	v_sub_f32_e32 v1, s53, v23
	v_mul_f32_e32 v1, 0x3fb8aa3b, v1
	v_exp_f32_e32 v1, v1
	s_waitcnt vmcnt(1)
	v_lshlrev_b32_e32 v99, 16, v8
	v_mul_f32_e32 v0, v0, v99
	v_and_b32_e32 v8, 0xffff0000, v8
	v_cvt_pk_bf16_f32 v0, v0, s0
	ds_write_b16 v54, v0 offset:1024
	v_mul_f32_e32 v0, v1, v8
	v_cvt_pk_bf16_f32 v0, v0, s0
	ds_write_b16 v54, v0 offset:1152
	v_sub_f32_e32 v0, s54, v24
	v_mul_f32_e32 v0, 0x3fb8aa3b, v0
	v_exp_f32_e32 v0, v0
	v_sub_f32_e32 v1, s56, v25
	v_mul_f32_e32 v1, 0x3fb8aa3b, v1
	v_exp_f32_e32 v1, v1
	v_lshlrev_b32_e32 v100, 16, v9
	v_mul_f32_e32 v0, v0, v100
	v_and_b32_e32 v9, 0xffff0000, v9
	v_cvt_pk_bf16_f32 v0, v0, s0
	ds_write_b16 v54, v0 offset:1280
	v_mul_f32_e32 v0, v1, v9
	v_cvt_pk_bf16_f32 v0, v0, s0
	ds_write_b16 v54, v0 offset:1408
	v_sub_f32_e32 v0, s55, v26
	v_mul_f32_e32 v0, 0x3fb8aa3b, v0
	v_exp_f32_e32 v0, v0
	v_sub_f32_e32 v1, s57, v27
	v_mul_f32_e32 v1, 0x3fb8aa3b, v1
	v_exp_f32_e32 v1, v1
	v_lshlrev_b32_e32 v101, 16, v10
	v_mul_f32_e32 v0, v0, v101
	v_and_b32_e32 v10, 0xffff0000, v10
	v_cvt_pk_bf16_f32 v0, v0, s0
	ds_write_b16 v54, v0 offset:1536
	v_mul_f32_e32 v0, v1, v10
	v_cvt_pk_bf16_f32 v0, v0, s0
	ds_write_b16 v54, v0 offset:1664
	v_sub_f32_e32 v0, s58, v28
	v_mul_f32_e32 v0, 0x3fb8aa3b, v0
	v_exp_f32_e32 v0, v0
	v_sub_f32_e32 v1, s59, v29
	v_mul_f32_e32 v1, 0x3fb8aa3b, v1
	v_exp_f32_e32 v1, v1
	v_lshlrev_b32_e32 v102, 16, v11
	v_mul_f32_e32 v0, v0, v102
	v_and_b32_e32 v11, 0xffff0000, v11
	v_cvt_pk_bf16_f32 v0, v0, s0
	ds_write_b16 v54, v0 offset:1792
	v_mul_f32_e32 v0, v1, v11
	v_cvt_pk_bf16_f32 v0, v0, s0
	ds_write_b16 v54, v0 offset:1920
	v_sub_f32_e32 v0, s60, v30
	v_mul_f32_e32 v0, 0x3fb8aa3b, v0
	v_exp_f32_e32 v0, v0
	v_sub_f32_e32 v1, s61, v31
	v_mul_f32_e32 v1, 0x3fb8aa3b, v1
	v_exp_f32_e32 v1, v1
	v_lshlrev_b32_e32 v103, 16, v4
	v_mul_f32_e32 v0, v0, v103
	v_and_b32_e32 v4, 0xffff0000, v4
	v_cvt_pk_bf16_f32 v0, v0, s0
	ds_write_b16 v54, v0 offset:2048
	v_mul_f32_e32 v0, v1, v4
	v_cvt_pk_bf16_f32 v0, v0, s0
	ds_write_b16 v54, v0 offset:2176
	v_sub_f32_e32 v0, s62, v76
	v_mul_f32_e32 v0, 0x3fb8aa3b, v0
	v_exp_f32_e32 v0, v0
	v_sub_f32_e32 v1, s63, v77
	v_mul_f32_e32 v1, 0x3fb8aa3b, v1
	v_exp_f32_e32 v1, v1
	v_lshlrev_b32_e32 v104, 16, v5
	v_mul_f32_e32 v0, v0, v104
	v_and_b32_e32 v5, 0xffff0000, v5
	v_cvt_pk_bf16_f32 v0, v0, s0
	ds_write_b16 v54, v0 offset:2304
	v_mul_f32_e32 v0, v1, v5
	v_cvt_pk_bf16_f32 v0, v0, s0
	v_readlane_b32 s64, v78, 63
	ds_write_b16 v54, v0 offset:2432
	v_readlane_b32 s65, v79, 63
	v_sub_f32_e32 v0, s64, v78
	v_mul_f32_e32 v0, 0x3fb8aa3b, v0
	v_exp_f32_e32 v0, v0
	v_sub_f32_e32 v1, s65, v79
	v_mul_f32_e32 v1, 0x3fb8aa3b, v1
	v_exp_f32_e32 v1, v1
	v_lshlrev_b32_e32 v105, 16, v6
	v_mul_f32_e32 v0, v0, v105
	v_and_b32_e32 v6, 0xffff0000, v6
	v_cvt_pk_bf16_f32 v0, v0, s0
	ds_write_b16 v54, v0 offset:2560
	v_mul_f32_e32 v0, v1, v6
	v_cvt_pk_bf16_f32 v0, v0, s0
	v_readlane_b32 s66, v81, 63
	ds_write_b16 v54, v0 offset:2688
	v_readlane_b32 s67, v82, 63
	v_sub_f32_e32 v0, s66, v81
	v_mul_f32_e32 v0, 0x3fb8aa3b, v0
	v_exp_f32_e32 v0, v0
	v_sub_f32_e32 v1, s67, v82
	v_mul_f32_e32 v1, 0x3fb8aa3b, v1
	v_exp_f32_e32 v1, v1
	v_lshlrev_b32_e32 v106, 16, v7
	v_mul_f32_e32 v0, v0, v106
	v_and_b32_e32 v7, 0xffff0000, v7
	v_cvt_pk_bf16_f32 v0, v0, s0
	ds_write_b16 v54, v0 offset:2816
	v_mul_f32_e32 v0, v1, v7
	v_cvt_pk_bf16_f32 v0, v0, s0
	v_readlane_b32 s68, v80, 63
	ds_write_b16 v54, v0 offset:2944
	v_readlane_b32 s69, v83, 63
	v_sub_f32_e32 v0, s68, v80
	v_mul_f32_e32 v0, 0x3fb8aa3b, v0
	v_exp_f32_e32 v0, v0
	v_sub_f32_e32 v1, s69, v83
	v_mul_f32_e32 v1, 0x3fb8aa3b, v1
	v_exp_f32_e32 v1, v1
	s_waitcnt vmcnt(0)
	v_lshlrev_b32_e32 v107, 16, v14
	v_mul_f32_e32 v0, v0, v107
	v_and_b32_e32 v14, 0xffff0000, v14
	v_cvt_pk_bf16_f32 v0, v0, s0
	ds_write_b16 v54, v0 offset:3072
	v_mul_f32_e32 v0, v1, v14
	v_cvt_pk_bf16_f32 v0, v0, s0
	v_readlane_b32 s70, v84, 63
	ds_write_b16 v54, v0 offset:3200
	v_readlane_b32 s71, v85, 63
	v_sub_f32_e32 v0, s70, v84
	v_mul_f32_e32 v0, 0x3fb8aa3b, v0
	v_exp_f32_e32 v0, v0
	v_sub_f32_e32 v1, s71, v85
	v_mul_f32_e32 v1, 0x3fb8aa3b, v1
	v_exp_f32_e32 v1, v1
	v_lshlrev_b32_e32 v108, 16, v15
	v_mul_f32_e32 v0, v0, v108
	v_and_b32_e32 v15, 0xffff0000, v15
	v_cvt_pk_bf16_f32 v0, v0, s0
	ds_write_b16 v54, v0 offset:3328
	v_mul_f32_e32 v0, v1, v15
	v_cvt_pk_bf16_f32 v0, v0, s0
	v_readlane_b32 s72, v86, 63
	ds_write_b16 v54, v0 offset:3456
	v_readlane_b32 s73, v87, 63
	v_sub_f32_e32 v0, s72, v86
	v_mul_f32_e32 v0, 0x3fb8aa3b, v0
	v_exp_f32_e32 v0, v0
	v_sub_f32_e32 v1, s73, v87
	v_mul_f32_e32 v1, 0x3fb8aa3b, v1
	v_exp_f32_e32 v1, v1
	v_lshlrev_b32_e32 v109, 16, v16
	v_mul_f32_e32 v0, v0, v109
	v_and_b32_e32 v16, 0xffff0000, v16
	v_cvt_pk_bf16_f32 v0, v0, s0
	ds_write_b16 v54, v0 offset:3584
	v_mul_f32_e32 v0, v1, v16
	v_cvt_pk_bf16_f32 v0, v0, s0
	v_readlane_b32 s74, v88, 63
	ds_write_b16 v54, v0 offset:3712
	v_readlane_b32 s75, v89, 63
	v_sub_f32_e32 v0, s74, v88
	v_mul_f32_e32 v0, 0x3fb8aa3b, v0
	v_exp_f32_e32 v0, v0
	v_sub_f32_e32 v1, s75, v89
	v_mul_f32_e32 v1, 0x3fb8aa3b, v1
	v_exp_f32_e32 v1, v1
	v_lshlrev_b32_e32 v110, 16, v17
	v_mul_f32_e32 v0, v0, v110
	v_and_b32_e32 v17, 0xffff0000, v17
	v_cvt_pk_bf16_f32 v0, v0, s0
	ds_write_b16 v54, v0 offset:3840
	v_mul_f32_e32 v0, v1, v17
	v_cvt_pk_bf16_f32 v0, v0, s0
	ds_write_b16 v54, v0 offset:3968
	s_and_saveexec_b64 s[30:31], s[46:47]
	s_cbranch_execz .LBB0_346
	v_mov_b32_e32 v0, s15
	v_cndmask_b32_e64 v0, 0, v0, s[38:39]
	v_mov_b32_e32 v1, s19
	v_cndmask_b32_e64 v0, v0, v1, s[12:13]
	v_mov_b32_e32 v1, vcc_hi
	v_cndmask_b32_e64 v0, v0, v1, s[10:11]
	v_mov_b32_e32 v1, s48
	v_cndmask_b32_e64 v0, v0, v1, s[8:9]
	v_mov_b32_e32 v1, s50
	v_cndmask_b32_e64 v0, v0, v1, s[6:7]
	v_mov_b32_e32 v1, vcc_lo
	v_cndmask_b32_e64 v0, v0, v1, s[4:5]
	v_mov_b32_e32 v1, s49
	v_cndmask_b32_e64 v0, v0, v1, s[2:3]
	v_mov_b32_e32 v1, s51
	v_cndmask_b32_e64 v0, v0, v1, s[96:97]
	v_mov_b32_e32 v1, s52
	v_cndmask_b32_e64 v0, v0, v1, s[94:95]
	v_mov_b32_e32 v1, s53
	v_cndmask_b32_e64 v0, v0, v1, s[92:93]
	v_mov_b32_e32 v1, s54
	v_cndmask_b32_e64 v0, v0, v1, s[90:91]
	v_mov_b32_e32 v1, s56
	v_cndmask_b32_e64 v0, v0, v1, s[88:89]
	v_mov_b32_e32 v1, s55
	v_cndmask_b32_e64 v0, v0, v1, s[78:79]
	v_mov_b32_e32 v1, s57
	v_cndmask_b32_e64 v0, v0, v1, s[84:85]
	v_mov_b32_e32 v1, s58
	v_cndmask_b32_e64 v0, v0, v1, s[82:83]
	v_mov_b32_e32 v1, s59
	v_readlane_b32 s48, v255, 11
	v_cndmask_b32_e64 v0, v0, v1, s[80:81]
	v_mov_b32_e32 v1, s60
	v_readlane_b32 s49, v255, 12
	s_nop 1
	v_cndmask_b32_e64 v0, v0, v1, s[48:49]
	v_readlane_b32 s48, v255, 9
	v_mov_b32_e32 v1, s61
	v_readlane_b32 s49, v255, 10
	s_nop 1
	v_cndmask_b32_e64 v0, v0, v1, s[48:49]
	v_readlane_b32 s48, v255, 7
	v_mov_b32_e32 v1, s62
	v_readlane_b32 s49, v255, 8
	s_nop 1
	v_cndmask_b32_e64 v0, v0, v1, s[48:49]
	v_readlane_b32 s48, v255, 5
	v_mov_b32_e32 v1, s63
	v_readlane_b32 s49, v255, 6
	s_nop 1
	v_cndmask_b32_e64 v0, v0, v1, s[48:49]
	v_readlane_b32 s48, v255, 3
	v_mov_b32_e32 v1, s64
	v_readlane_b32 s49, v255, 4
	s_nop 1
	v_cndmask_b32_e64 v0, v0, v1, s[48:49]
	v_readlane_b32 s48, v255, 1
	v_mov_b32_e32 v1, s65
	v_readlane_b32 s49, v255, 2
	s_nop 1
	v_cndmask_b32_e64 v0, v0, v1, s[48:49]
	v_readlane_b32 s48, v254, 63
	v_mov_b32_e32 v1, s66
	v_readlane_b32 s49, v255, 0
	s_nop 1
	v_cndmask_b32_e64 v0, v0, v1, s[48:49]
	v_readlane_b32 s48, v254, 61
	v_mov_b32_e32 v1, s67
	v_readlane_b32 s49, v254, 62
	s_nop 1
	v_cndmask_b32_e64 v0, v0, v1, s[48:49]
	v_readlane_b32 s48, v254, 59
	v_mov_b32_e32 v1, s68
	v_readlane_b32 s49, v254, 60
	s_nop 1
	v_cndmask_b32_e64 v0, v0, v1, s[48:49]
	v_readlane_b32 s48, v254, 57
	v_mov_b32_e32 v1, s69
	v_readlane_b32 s49, v254, 58
	s_nop 1
	v_cndmask_b32_e64 v0, v0, v1, s[48:49]
	v_readlane_b32 s48, v254, 55
	v_mov_b32_e32 v1, s70
	v_readlane_b32 s49, v254, 56
	s_nop 1
	v_cndmask_b32_e64 v0, v0, v1, s[48:49]
	v_readlane_b32 s48, v254, 53
	v_mov_b32_e32 v1, s71
	v_readlane_b32 s49, v254, 54
	s_nop 1
	v_cndmask_b32_e64 v0, v0, v1, s[48:49]
	v_readlane_b32 s48, v254, 51
	v_mov_b32_e32 v1, s72
	v_readlane_b32 s49, v254, 52
	s_nop 1
	v_cndmask_b32_e64 v0, v0, v1, s[48:49]
	v_readlane_b32 s48, v254, 49
	v_mov_b32_e32 v1, s73
	v_readlane_b32 s49, v254, 50
	s_nop 1
	v_cndmask_b32_e64 v0, v0, v1, s[48:49]
	v_readlane_b32 s48, v254, 47
	v_mov_b32_e32 v1, s74
	v_readlane_b32 s49, v254, 48
	s_nop 1
	v_cndmask_b32_e64 v0, v0, v1, s[48:49]
	v_readlane_b32 s48, v254, 45
	v_mov_b32_e32 v1, s75
	v_readlane_b32 s49, v254, 46
	s_nop 1
	v_cndmask_b32_e64 v2, v0, v1, s[48:49]
	v_mul_f32_e32 v2, 0x3fb8aa3b, v2
	v_exp_f32_e32 v2, v2
	v_lshl_or_b32 v0, s14, 7, v55
	v_ashrrev_i32_e32 v1, 31, v0
	v_lshl_add_u64 v[0:1], v[0:1], 2, s[24:25]
	global_store_dword v[0:1], v2, off
	s_branch .LBB0_346

.LBB0_768:
	s_ashr_i32 s2, s16, 2
	s_ashr_i32 s3, s2, 31
	s_lshl_b64 s[14:15], s[2:3], 6
	v_mov_b32_e32 v1, s15
	v_or_b32_e32 v0, s14, v100
	v_lshlrev_b64 v[28:29], 9, v[0:1]
	v_lshl_add_u64 v[12:13], s[6:7], 0, v[28:29]
	global_load_dwordx4 v[16:19], v[12:13], off offset:48
	global_load_dwordx4 v[20:23], v[12:13], off offset:32
	global_load_dwordx4 v[24:27], v[12:13], off offset:16
	global_load_dwordx4 v[30:33], v[12:13], off
	global_load_dwordx4 v[0:3], v[12:13], off offset:112
	global_load_dwordx4 v[4:7], v[12:13], off offset:96
	global_load_dwordx4 v[8:11], v[12:13], off offset:80
	s_nop 0
	global_load_dwordx4 v[12:15], v[12:13], off offset:64
	s_waitcnt vmcnt(6)
	s_nop 1
	v_add_f32_dpp v20, v20, v20 row_shr:1 row_mask:0xf bank_mask:0xf bound_ctrl:0
	v_add_f32_dpp v21, v21, v21 row_shr:1 row_mask:0xf bank_mask:0xf bound_ctrl:0
	v_add_f32_dpp v22, v22, v22 row_shr:1 row_mask:0xf bank_mask:0xf bound_ctrl:0
	v_add_f32_dpp v23, v23, v23 row_shr:1 row_mask:0xf bank_mask:0xf bound_ctrl:0
	v_add_f32_dpp v16, v16, v16 row_shr:1 row_mask:0xf bank_mask:0xf bound_ctrl:0
	v_add_f32_dpp v17, v17, v17 row_shr:1 row_mask:0xf bank_mask:0xf bound_ctrl:0
	v_add_f32_dpp v18, v18, v18 row_shr:1 row_mask:0xf bank_mask:0xf bound_ctrl:0
	v_add_f32_dpp v19, v19, v19 row_shr:1 row_mask:0xf bank_mask:0xf bound_ctrl:0
	v_add_f32_dpp v20, v20, v20 row_shr:2 row_mask:0xf bank_mask:0xf bound_ctrl:0
	v_add_f32_dpp v21, v21, v21 row_shr:2 row_mask:0xf bank_mask:0xf bound_ctrl:0
	v_add_f32_dpp v22, v22, v22 row_shr:2 row_mask:0xf bank_mask:0xf bound_ctrl:0
	v_add_f32_dpp v23, v23, v23 row_shr:2 row_mask:0xf bank_mask:0xf bound_ctrl:0
	v_add_f32_dpp v16, v16, v16 row_shr:2 row_mask:0xf bank_mask:0xf bound_ctrl:0
	v_add_f32_dpp v17, v17, v17 row_shr:2 row_mask:0xf bank_mask:0xf bound_ctrl:0
	v_add_f32_dpp v18, v18, v18 row_shr:2 row_mask:0xf bank_mask:0xf bound_ctrl:0
	v_add_f32_dpp v19, v19, v19 row_shr:2 row_mask:0xf bank_mask:0xf bound_ctrl:0
	v_add_f32_dpp v20, v20, v20 row_shr:4 row_mask:0xf bank_mask:0xf bound_ctrl:0
	v_add_f32_dpp v21, v21, v21 row_shr:4 row_mask:0xf bank_mask:0xf bound_ctrl:0
	v_add_f32_dpp v22, v22, v22 row_shr:4 row_mask:0xf bank_mask:0xf bound_ctrl:0
	v_add_f32_dpp v23, v23, v23 row_shr:4 row_mask:0xf bank_mask:0xf bound_ctrl:0
	v_add_f32_dpp v16, v16, v16 row_shr:4 row_mask:0xf bank_mask:0xf bound_ctrl:0
	v_add_f32_dpp v17, v17, v17 row_shr:4 row_mask:0xf bank_mask:0xf bound_ctrl:0
	v_add_f32_dpp v18, v18, v18 row_shr:4 row_mask:0xf bank_mask:0xf bound_ctrl:0
	v_add_f32_dpp v19, v19, v19 row_shr:4 row_mask:0xf bank_mask:0xf bound_ctrl:0
	v_add_f32_dpp v20, v20, v20 row_shr:8 row_mask:0xf bank_mask:0xf bound_ctrl:0
	v_add_f32_dpp v21, v21, v21 row_shr:8 row_mask:0xf bank_mask:0xf bound_ctrl:0
	v_add_f32_dpp v22, v22, v22 row_shr:8 row_mask:0xf bank_mask:0xf bound_ctrl:0
	v_add_f32_dpp v23, v23, v23 row_shr:8 row_mask:0xf bank_mask:0xf bound_ctrl:0
	v_add_f32_dpp v16, v16, v16 row_shr:8 row_mask:0xf bank_mask:0xf bound_ctrl:0
	v_add_f32_dpp v17, v17, v17 row_shr:8 row_mask:0xf bank_mask:0xf bound_ctrl:0
	v_add_f32_dpp v18, v18, v18 row_shr:8 row_mask:0xf bank_mask:0xf bound_ctrl:0
	v_add_f32_dpp v19, v19, v19 row_shr:8 row_mask:0xf bank_mask:0xf bound_ctrl:0
	v_add_f32_dpp v20, v20, v20 row_bcast:15 row_mask:0xa bank_mask:0xf
	v_add_f32_dpp v21, v21, v21 row_bcast:15 row_mask:0xa bank_mask:0xf
	v_add_f32_dpp v22, v22, v22 row_bcast:15 row_mask:0xa bank_mask:0xf
	v_add_f32_dpp v23, v23, v23 row_bcast:15 row_mask:0xa bank_mask:0xf
	v_add_f32_dpp v16, v16, v16 row_bcast:15 row_mask:0xa bank_mask:0xf
	v_add_f32_dpp v17, v17, v17 row_bcast:15 row_mask:0xa bank_mask:0xf
	v_add_f32_dpp v18, v18, v18 row_bcast:15 row_mask:0xa bank_mask:0xf
	v_add_f32_dpp v19, v19, v19 row_bcast:15 row_mask:0xa bank_mask:0xf
	v_add_f32_dpp v20, v20, v20 row_bcast:31 row_mask:0xc bank_mask:0xf
	v_add_f32_dpp v21, v21, v21 row_bcast:31 row_mask:0xc bank_mask:0xf
	v_add_f32_dpp v22, v22, v22 row_bcast:31 row_mask:0xc bank_mask:0xf
	v_add_f32_dpp v23, v23, v23 row_bcast:31 row_mask:0xc bank_mask:0xf
	v_add_f32_dpp v16, v16, v16 row_bcast:31 row_mask:0xc bank_mask:0xf
	v_add_f32_dpp v17, v17, v17 row_bcast:31 row_mask:0xc bank_mask:0xf
	v_add_f32_dpp v18, v18, v18 row_bcast:31 row_mask:0xc bank_mask:0xf
	v_add_f32_dpp v19, v19, v19 row_bcast:31 row_mask:0xc bank_mask:0xf
	s_waitcnt vmcnt(4)
	s_nop 1
	v_add_f32_dpp v30, v30, v30 row_shr:1 row_mask:0xf bank_mask:0xf bound_ctrl:0
	v_add_f32_dpp v31, v31, v31 row_shr:1 row_mask:0xf bank_mask:0xf bound_ctrl:0
	v_add_f32_dpp v32, v32, v32 row_shr:1 row_mask:0xf bank_mask:0xf bound_ctrl:0
	v_add_f32_dpp v33, v33, v33 row_shr:1 row_mask:0xf bank_mask:0xf bound_ctrl:0
	v_add_f32_dpp v24, v24, v24 row_shr:1 row_mask:0xf bank_mask:0xf bound_ctrl:0
	v_add_f32_dpp v25, v25, v25 row_shr:1 row_mask:0xf bank_mask:0xf bound_ctrl:0
	v_add_f32_dpp v26, v26, v26 row_shr:1 row_mask:0xf bank_mask:0xf bound_ctrl:0
	v_add_f32_dpp v27, v27, v27 row_shr:1 row_mask:0xf bank_mask:0xf bound_ctrl:0
	v_add_f32_dpp v30, v30, v30 row_shr:2 row_mask:0xf bank_mask:0xf bound_ctrl:0
	v_add_f32_dpp v31, v31, v31 row_shr:2 row_mask:0xf bank_mask:0xf bound_ctrl:0
	v_add_f32_dpp v32, v32, v32 row_shr:2 row_mask:0xf bank_mask:0xf bound_ctrl:0
	v_add_f32_dpp v33, v33, v33 row_shr:2 row_mask:0xf bank_mask:0xf bound_ctrl:0
	v_add_f32_dpp v24, v24, v24 row_shr:2 row_mask:0xf bank_mask:0xf bound_ctrl:0
	v_add_f32_dpp v25, v25, v25 row_shr:2 row_mask:0xf bank_mask:0xf bound_ctrl:0
	v_add_f32_dpp v26, v26, v26 row_shr:2 row_mask:0xf bank_mask:0xf bound_ctrl:0
	v_add_f32_dpp v27, v27, v27 row_shr:2 row_mask:0xf bank_mask:0xf bound_ctrl:0
	v_add_f32_dpp v30, v30, v30 row_shr:4 row_mask:0xf bank_mask:0xf bound_ctrl:0
	v_add_f32_dpp v31, v31, v31 row_shr:4 row_mask:0xf bank_mask:0xf bound_ctrl:0
	v_add_f32_dpp v32, v32, v32 row_shr:4 row_mask:0xf bank_mask:0xf bound_ctrl:0
	v_add_f32_dpp v33, v33, v33 row_shr:4 row_mask:0xf bank_mask:0xf bound_ctrl:0
	v_add_f32_dpp v24, v24, v24 row_shr:4 row_mask:0xf bank_mask:0xf bound_ctrl:0
	v_add_f32_dpp v25, v25, v25 row_shr:4 row_mask:0xf bank_mask:0xf bound_ctrl:0
	v_add_f32_dpp v26, v26, v26 row_shr:4 row_mask:0xf bank_mask:0xf bound_ctrl:0
	v_add_f32_dpp v27, v27, v27 row_shr:4 row_mask:0xf bank_mask:0xf bound_ctrl:0
	v_add_f32_dpp v30, v30, v30 row_shr:8 row_mask:0xf bank_mask:0xf bound_ctrl:0
	v_add_f32_dpp v31, v31, v31 row_shr:8 row_mask:0xf bank_mask:0xf bound_ctrl:0
	v_add_f32_dpp v32, v32, v32 row_shr:8 row_mask:0xf bank_mask:0xf bound_ctrl:0
	v_add_f32_dpp v33, v33, v33 row_shr:8 row_mask:0xf bank_mask:0xf bound_ctrl:0
	v_add_f32_dpp v24, v24, v24 row_shr:8 row_mask:0xf bank_mask:0xf bound_ctrl:0
	v_add_f32_dpp v25, v25, v25 row_shr:8 row_mask:0xf bank_mask:0xf bound_ctrl:0
	v_add_f32_dpp v26, v26, v26 row_shr:8 row_mask:0xf bank_mask:0xf bound_ctrl:0
	v_add_f32_dpp v27, v27, v27 row_shr:8 row_mask:0xf bank_mask:0xf bound_ctrl:0
	v_add_f32_dpp v30, v30, v30 row_bcast:15 row_mask:0xa bank_mask:0xf
	v_add_f32_dpp v31, v31, v31 row_bcast:15 row_mask:0xa bank_mask:0xf
	v_add_f32_dpp v32, v32, v32 row_bcast:15 row_mask:0xa bank_mask:0xf
	v_add_f32_dpp v33, v33, v33 row_bcast:15 row_mask:0xa bank_mask:0xf
	v_add_f32_dpp v24, v24, v24 row_bcast:15 row_mask:0xa bank_mask:0xf
	v_add_f32_dpp v25, v25, v25 row_bcast:15 row_mask:0xa bank_mask:0xf
	v_add_f32_dpp v26, v26, v26 row_bcast:15 row_mask:0xa bank_mask:0xf
	v_add_f32_dpp v27, v27, v27 row_bcast:15 row_mask:0xa bank_mask:0xf
	v_add_f32_dpp v30, v30, v30 row_bcast:31 row_mask:0xc bank_mask:0xf
	v_add_f32_dpp v31, v31, v31 row_bcast:31 row_mask:0xc bank_mask:0xf
	v_add_f32_dpp v32, v32, v32 row_bcast:31 row_mask:0xc bank_mask:0xf
	v_add_f32_dpp v33, v33, v33 row_bcast:31 row_mask:0xc bank_mask:0xf
	v_add_f32_dpp v24, v24, v24 row_bcast:31 row_mask:0xc bank_mask:0xf
	v_add_f32_dpp v25, v25, v25 row_bcast:31 row_mask:0xc bank_mask:0xf
	v_add_f32_dpp v26, v26, v26 row_bcast:31 row_mask:0xc bank_mask:0xf
	v_add_f32_dpp v27, v27, v27 row_bcast:31 row_mask:0xc bank_mask:0xf
	s_waitcnt vmcnt(2)
	s_nop 1
	v_add_f32_dpp v4, v4, v4 row_shr:1 row_mask:0xf bank_mask:0xf bound_ctrl:0
	v_add_f32_dpp v5, v5, v5 row_shr:1 row_mask:0xf bank_mask:0xf bound_ctrl:0
	v_add_f32_dpp v6, v6, v6 row_shr:1 row_mask:0xf bank_mask:0xf bound_ctrl:0
	v_add_f32_dpp v7, v7, v7 row_shr:1 row_mask:0xf bank_mask:0xf bound_ctrl:0
	v_add_f32_dpp v0, v0, v0 row_shr:1 row_mask:0xf bank_mask:0xf bound_ctrl:0
	v_add_f32_dpp v1, v1, v1 row_shr:1 row_mask:0xf bank_mask:0xf bound_ctrl:0
	v_add_f32_dpp v2, v2, v2 row_shr:1 row_mask:0xf bank_mask:0xf bound_ctrl:0
	v_add_f32_dpp v3, v3, v3 row_shr:1 row_mask:0xf bank_mask:0xf bound_ctrl:0
	v_add_f32_dpp v4, v4, v4 row_shr:2 row_mask:0xf bank_mask:0xf bound_ctrl:0
	v_add_f32_dpp v5, v5, v5 row_shr:2 row_mask:0xf bank_mask:0xf bound_ctrl:0
	v_add_f32_dpp v6, v6, v6 row_shr:2 row_mask:0xf bank_mask:0xf bound_ctrl:0
	v_add_f32_dpp v7, v7, v7 row_shr:2 row_mask:0xf bank_mask:0xf bound_ctrl:0
	v_add_f32_dpp v0, v0, v0 row_shr:2 row_mask:0xf bank_mask:0xf bound_ctrl:0
	v_add_f32_dpp v1, v1, v1 row_shr:2 row_mask:0xf bank_mask:0xf bound_ctrl:0
	v_add_f32_dpp v2, v2, v2 row_shr:2 row_mask:0xf bank_mask:0xf bound_ctrl:0
	v_add_f32_dpp v3, v3, v3 row_shr:2 row_mask:0xf bank_mask:0xf bound_ctrl:0
	v_add_f32_dpp v4, v4, v4 row_shr:4 row_mask:0xf bank_mask:0xf bound_ctrl:0
	v_add_f32_dpp v5, v5, v5 row_shr:4 row_mask:0xf bank_mask:0xf bound_ctrl:0
	v_add_f32_dpp v6, v6, v6 row_shr:4 row_mask:0xf bank_mask:0xf bound_ctrl:0
	v_add_f32_dpp v7, v7, v7 row_shr:4 row_mask:0xf bank_mask:0xf bound_ctrl:0
	v_add_f32_dpp v0, v0, v0 row_shr:4 row_mask:0xf bank_mask:0xf bound_ctrl:0
	v_add_f32_dpp v1, v1, v1 row_shr:4 row_mask:0xf bank_mask:0xf bound_ctrl:0
	v_add_f32_dpp v2, v2, v2 row_shr:4 row_mask:0xf bank_mask:0xf bound_ctrl:0
	v_add_f32_dpp v3, v3, v3 row_shr:4 row_mask:0xf bank_mask:0xf bound_ctrl:0
	v_add_f32_dpp v4, v4, v4 row_shr:8 row_mask:0xf bank_mask:0xf bound_ctrl:0
	v_add_f32_dpp v5, v5, v5 row_shr:8 row_mask:0xf bank_mask:0xf bound_ctrl:0
	v_add_f32_dpp v6, v6, v6 row_shr:8 row_mask:0xf bank_mask:0xf bound_ctrl:0
	v_add_f32_dpp v7, v7, v7 row_shr:8 row_mask:0xf bank_mask:0xf bound_ctrl:0
	v_add_f32_dpp v0, v0, v0 row_shr:8 row_mask:0xf bank_mask:0xf bound_ctrl:0
	v_add_f32_dpp v1, v1, v1 row_shr:8 row_mask:0xf bank_mask:0xf bound_ctrl:0
	v_add_f32_dpp v2, v2, v2 row_shr:8 row_mask:0xf bank_mask:0xf bound_ctrl:0
	v_add_f32_dpp v3, v3, v3 row_shr:8 row_mask:0xf bank_mask:0xf bound_ctrl:0
	v_add_f32_dpp v4, v4, v4 row_bcast:15 row_mask:0xa bank_mask:0xf
	v_add_f32_dpp v5, v5, v5 row_bcast:15 row_mask:0xa bank_mask:0xf
	v_add_f32_dpp v6, v6, v6 row_bcast:15 row_mask:0xa bank_mask:0xf
	v_add_f32_dpp v7, v7, v7 row_bcast:15 row_mask:0xa bank_mask:0xf
	v_add_f32_dpp v0, v0, v0 row_bcast:15 row_mask:0xa bank_mask:0xf
	v_add_f32_dpp v1, v1, v1 row_bcast:15 row_mask:0xa bank_mask:0xf
	v_add_f32_dpp v2, v2, v2 row_bcast:15 row_mask:0xa bank_mask:0xf
	v_add_f32_dpp v3, v3, v3 row_bcast:15 row_mask:0xa bank_mask:0xf
	v_add_f32_dpp v4, v4, v4 row_bcast:31 row_mask:0xc bank_mask:0xf
	v_add_f32_dpp v5, v5, v5 row_bcast:31 row_mask:0xc bank_mask:0xf
	v_add_f32_dpp v6, v6, v6 row_bcast:31 row_mask:0xc bank_mask:0xf
	v_add_f32_dpp v7, v7, v7 row_bcast:31 row_mask:0xc bank_mask:0xf
	v_add_f32_dpp v0, v0, v0 row_bcast:31 row_mask:0xc bank_mask:0xf
	v_add_f32_dpp v1, v1, v1 row_bcast:31 row_mask:0xc bank_mask:0xf
	v_add_f32_dpp v2, v2, v2 row_bcast:31 row_mask:0xc bank_mask:0xf
	v_add_f32_dpp v3, v3, v3 row_bcast:31 row_mask:0xc bank_mask:0xf
	s_waitcnt vmcnt(0)
	s_nop 1
	v_add_f32_dpp v12, v12, v12 row_shr:1 row_mask:0xf bank_mask:0xf bound_ctrl:0
	v_add_f32_dpp v13, v13, v13 row_shr:1 row_mask:0xf bank_mask:0xf bound_ctrl:0
	v_add_f32_dpp v14, v14, v14 row_shr:1 row_mask:0xf bank_mask:0xf bound_ctrl:0
	v_add_f32_dpp v15, v15, v15 row_shr:1 row_mask:0xf bank_mask:0xf bound_ctrl:0
	v_add_f32_dpp v8, v8, v8 row_shr:1 row_mask:0xf bank_mask:0xf bound_ctrl:0
	v_add_f32_dpp v9, v9, v9 row_shr:1 row_mask:0xf bank_mask:0xf bound_ctrl:0
	v_add_f32_dpp v10, v10, v10 row_shr:1 row_mask:0xf bank_mask:0xf bound_ctrl:0
	v_add_f32_dpp v11, v11, v11 row_shr:1 row_mask:0xf bank_mask:0xf bound_ctrl:0
	v_add_f32_dpp v12, v12, v12 row_shr:2 row_mask:0xf bank_mask:0xf bound_ctrl:0
	v_add_f32_dpp v13, v13, v13 row_shr:2 row_mask:0xf bank_mask:0xf bound_ctrl:0
	v_add_f32_dpp v14, v14, v14 row_shr:2 row_mask:0xf bank_mask:0xf bound_ctrl:0
	v_add_f32_dpp v15, v15, v15 row_shr:2 row_mask:0xf bank_mask:0xf bound_ctrl:0
	v_add_f32_dpp v8, v8, v8 row_shr:2 row_mask:0xf bank_mask:0xf bound_ctrl:0
	v_add_f32_dpp v9, v9, v9 row_shr:2 row_mask:0xf bank_mask:0xf bound_ctrl:0
	v_add_f32_dpp v10, v10, v10 row_shr:2 row_mask:0xf bank_mask:0xf bound_ctrl:0
	v_add_f32_dpp v11, v11, v11 row_shr:2 row_mask:0xf bank_mask:0xf bound_ctrl:0
	v_add_f32_dpp v12, v12, v12 row_shr:4 row_mask:0xf bank_mask:0xf bound_ctrl:0
	v_add_f32_dpp v13, v13, v13 row_shr:4 row_mask:0xf bank_mask:0xf bound_ctrl:0
	v_add_f32_dpp v14, v14, v14 row_shr:4 row_mask:0xf bank_mask:0xf bound_ctrl:0
	v_add_f32_dpp v15, v15, v15 row_shr:4 row_mask:0xf bank_mask:0xf bound_ctrl:0
	v_add_f32_dpp v8, v8, v8 row_shr:4 row_mask:0xf bank_mask:0xf bound_ctrl:0
	v_add_f32_dpp v9, v9, v9 row_shr:4 row_mask:0xf bank_mask:0xf bound_ctrl:0
	v_add_f32_dpp v10, v10, v10 row_shr:4 row_mask:0xf bank_mask:0xf bound_ctrl:0
	v_add_f32_dpp v11, v11, v11 row_shr:4 row_mask:0xf bank_mask:0xf bound_ctrl:0
	v_add_f32_dpp v12, v12, v12 row_shr:8 row_mask:0xf bank_mask:0xf bound_ctrl:0
	v_add_f32_dpp v13, v13, v13 row_shr:8 row_mask:0xf bank_mask:0xf bound_ctrl:0
	v_add_f32_dpp v14, v14, v14 row_shr:8 row_mask:0xf bank_mask:0xf bound_ctrl:0
	v_add_f32_dpp v15, v15, v15 row_shr:8 row_mask:0xf bank_mask:0xf bound_ctrl:0
	v_add_f32_dpp v8, v8, v8 row_shr:8 row_mask:0xf bank_mask:0xf bound_ctrl:0
	v_add_f32_dpp v9, v9, v9 row_shr:8 row_mask:0xf bank_mask:0xf bound_ctrl:0
	v_add_f32_dpp v10, v10, v10 row_shr:8 row_mask:0xf bank_mask:0xf bound_ctrl:0
	v_add_f32_dpp v11, v11, v11 row_shr:8 row_mask:0xf bank_mask:0xf bound_ctrl:0
	v_add_f32_dpp v12, v12, v12 row_bcast:15 row_mask:0xa bank_mask:0xf
	v_add_f32_dpp v13, v13, v13 row_bcast:15 row_mask:0xa bank_mask:0xf
	v_add_f32_dpp v14, v14, v14 row_bcast:15 row_mask:0xa bank_mask:0xf
	v_add_f32_dpp v15, v15, v15 row_bcast:15 row_mask:0xa bank_mask:0xf
	v_add_f32_dpp v8, v8, v8 row_bcast:15 row_mask:0xa bank_mask:0xf
	v_add_f32_dpp v9, v9, v9 row_bcast:15 row_mask:0xa bank_mask:0xf
	v_add_f32_dpp v10, v10, v10 row_bcast:15 row_mask:0xa bank_mask:0xf
	v_add_f32_dpp v11, v11, v11 row_bcast:15 row_mask:0xa bank_mask:0xf
	v_add_f32_dpp v12, v12, v12 row_bcast:31 row_mask:0xc bank_mask:0xf
	v_add_f32_dpp v13, v13, v13 row_bcast:31 row_mask:0xc bank_mask:0xf
	v_add_f32_dpp v14, v14, v14 row_bcast:31 row_mask:0xc bank_mask:0xf
	v_add_f32_dpp v15, v15, v15 row_bcast:31 row_mask:0xc bank_mask:0xf
	v_add_f32_dpp v8, v8, v8 row_bcast:31 row_mask:0xc bank_mask:0xf
	v_add_f32_dpp v9, v9, v9 row_bcast:31 row_mask:0xc bank_mask:0xf
	v_add_f32_dpp v10, v10, v10 row_bcast:31 row_mask:0xc bank_mask:0xf
	v_add_f32_dpp v11, v11, v11 row_bcast:31 row_mask:0xc bank_mask:0xf
	v_mov_b32_e32 v37, v31
	v_mov_b32_e32 v35, v32
	v_mov_b32_e32 v38, v33
	v_mov_b32_e32 v36, v24
	v_mov_b32_e32 v39, v25
	v_mov_b32_e32 v40, v26
	v_mov_b32_e32 v41, v27
	v_mov_b32_e32 v42, v20
	v_mov_b32_e32 v43, v21
	v_mov_b32_e32 v46, v22
	v_mov_b32_e32 v48, v23
	v_mov_b32_e32 v47, v16
	v_mov_b32_e32 v49, v17
	v_mov_b32_e32 v52, v18
	v_mov_b32_e32 v53, v19
	v_mov_b32_e32 v50, v12
	v_mov_b32_e32 v51, v13
	v_mov_b32_e32 v54, v14
	v_mov_b32_e32 v56, v15
	v_mov_b32_e32 v55, v8
	v_mov_b32_e32 v57, v9
	v_mov_b32_e32 v60, v10
	v_mov_b32_e32 v61, v11
	v_mov_b32_e32 v58, v4
	v_mov_b32_e32 v59, v5
	v_mov_b32_e32 v62, v6
	v_mov_b32_e32 v65, v7
	v_mov_b32_e32 v63, v0
	v_mov_b32_e32 v66, v1
	v_mov_b32_e32 v64, v2
	v_mov_b32_e32 v67, v3
	s_nop 0
	v_add_u32_e32 v154, 0x3000, v149
	s_add_i32 s16, s16, s18
	v_mul_f32_e32 v30, 0x3fb8aa3b, v30
	v_exp_f32_e32 v30, v30
	s_waitcnt lgkmcnt(0)
	v_rcp_f32_e32 v44, v30
	s_waitcnt lgkmcnt(0)
	s_nop 0
	s_waitcnt lgkmcnt(0)
	s_nop 0
	s_waitcnt lgkmcnt(0)
	v_mul_f32_e32 v36, 0x3fb8aa3b, v36
	v_exp_f32_e32 v36, v36
	s_waitcnt lgkmcnt(0)
	s_nop 0
	s_waitcnt lgkmcnt(0)
	s_nop 0
	s_waitcnt lgkmcnt(0)
	s_nop 0
	s_waitcnt lgkmcnt(0)
	v_mul_f32_e32 v42, 0x3fb8aa3b, v42
	v_exp_f32_e32 v42, v42
	s_waitcnt lgkmcnt(0)
	v_mul_f32_e32 v43, 0x3fb8aa3b, v43
	v_exp_f32_e32 v43, v43
	s_waitcnt lgkmcnt(0)
	s_nop 0
	s_waitcnt lgkmcnt(0)
	s_nop 0
	s_waitcnt lgkmcnt(0)
	s_nop 0
	s_waitcnt lgkmcnt(0)
	s_nop 0
	s_waitcnt lgkmcnt(0)
	s_nop 0
	s_waitcnt lgkmcnt(0)
	s_nop 0
	s_waitcnt lgkmcnt(0)
	v_mul_f32_e32 v50, 0x3fb8aa3b, v50
	v_exp_f32_e32 v50, v50
	s_waitcnt lgkmcnt(0)
	v_mul_f32_e32 v51, 0x3fb8aa3b, v51
	v_exp_f32_e32 v51, v51
	s_waitcnt lgkmcnt(0)
	s_nop 0
	s_waitcnt lgkmcnt(0)
	s_nop 0
	s_waitcnt lgkmcnt(0)
	s_nop 0
	s_waitcnt lgkmcnt(0)
	s_nop 0
	s_waitcnt lgkmcnt(0)
	s_nop 0
	s_waitcnt lgkmcnt(0)
	s_nop 0
	s_waitcnt lgkmcnt(0)
	v_mul_f32_e32 v58, 0x3fb8aa3b, v58
	v_exp_f32_e32 v58, v58
	s_waitcnt lgkmcnt(0)
	v_lshl_add_u64 v[24:25], s[10:11], 0, v[28:29]
	v_mul_f32_e32 v59, 0x3fb8aa3b, v59
	v_exp_f32_e32 v59, v59
	v_lshl_add_u64 v[28:29], s[8:9], 0, v[28:29]
	s_waitcnt lgkmcnt(0)
	s_nop 0
	s_waitcnt lgkmcnt(0)
	s_nop 0
	s_waitcnt lgkmcnt(0)
	s_nop 0
	s_waitcnt lgkmcnt(0)
	v_mul_f32_e32 v31, 0x3fb8aa3b, v37
	v_exp_f32_e32 v31, v31
	v_mul_f32_e32 v37, 0x3fb8aa3b, v39
	v_exp_f32_e32 v37, v37
	s_waitcnt lgkmcnt(0)
	v_rcp_f32_e32 v45, v31
	v_pk_mul_f32 v[72:73], v[30:31], s[22:23] op_sel_hi:[1,0]
	s_waitcnt lgkmcnt(0)
	global_load_dwordx4 v[4:7], v[24:25], off offset:48
	global_load_dwordx4 v[12:15], v[24:25], off offset:32
	global_load_dwordx4 v[20:23], v[24:25], off offset:16
	global_load_dwordx4 v[68:71], v[24:25], off
	global_load_dwordx4 v[0:3], v[24:25], off offset:304
	global_load_dwordx4 v[8:11], v[24:25], off offset:288
	global_load_dwordx4 v[16:19], v[24:25], off offset:272
	s_nop 0
	global_load_dwordx4 v[24:27], v[24:25], off offset:256
	s_waitcnt vmcnt(4)
	v_lshlrev_b32_e32 v32, 16, v68
	v_and_b32_e32 v33, 0xffff0000, v68
	v_lshlrev_b32_e32 v34, 16, v69
	v_pk_mul_f32 v[32:33], v[72:73], v[32:33]
	s_waitcnt vmcnt(0)
	v_lshlrev_b32_e32 v30, 16, v24
	v_and_b32_e32 v31, 0xffff0000, v24
	v_mul_f32_e32 v24, 0x3fb8aa3b, v35
	v_pk_mul_f32 v[30:31], v[44:45], v[30:31]
	v_exp_f32_e32 v44, v24
	v_mul_f32_e32 v24, 0x3fb8aa3b, v38
	v_exp_f32_e32 v45, v24
	v_and_b32_e32 v35, 0xffff0000, v69
	v_rcp_f32_e32 v68, v44
	v_lshlrev_b32_e32 v24, 16, v25
	v_rcp_f32_e32 v69, v45
	v_pk_mul_f32 v[72:73], v[44:45], s[22:23] op_sel_hi:[1,0]
	v_rcp_f32_e32 v44, v36
	v_rcp_f32_e32 v45, v37
	v_and_b32_e32 v25, 0xffff0000, v25
	v_pk_mul_f32 v[24:25], v[68:69], v[24:25]
	v_pk_mul_f32 v[68:69], v[36:37], s[22:23] op_sel_hi:[1,0]
	v_lshlrev_b32_e32 v36, 16, v26
	v_and_b32_e32 v37, 0xffff0000, v26
	v_mul_f32_e32 v26, 0x3fb8aa3b, v40
	v_pk_mul_f32 v[36:37], v[44:45], v[36:37]
	v_exp_f32_e32 v44, v26
	v_mul_f32_e32 v26, 0x3fb8aa3b, v41
	v_exp_f32_e32 v45, v26
	v_lshlrev_b32_e32 v38, 16, v70
	v_and_b32_e32 v39, 0xffff0000, v70
	v_pk_mul_f32 v[38:39], v[68:69], v[38:39]
	v_rcp_f32_e32 v68, v44
	v_rcp_f32_e32 v69, v45
	v_lshlrev_b32_e32 v26, 16, v27
	v_and_b32_e32 v27, 0xffff0000, v27
	v_lshlrev_b32_e32 v40, 16, v71
	v_pk_mul_f32 v[26:27], v[68:69], v[26:27]
	v_rcp_f32_e32 v68, v42
	v_rcp_f32_e32 v69, v43
	v_and_b32_e32 v41, 0xffff0000, v71
	v_pk_mul_f32 v[70:71], v[44:45], s[22:23] op_sel_hi:[1,0]
	v_lshlrev_b32_e32 v44, 16, v20
	v_pk_mul_f32 v[40:41], v[70:71], v[40:41]
	v_pk_mul_f32 v[70:71], v[42:43], s[22:23] op_sel_hi:[1,0]
	v_lshlrev_b32_e32 v42, 16, v16
	v_and_b32_e32 v43, 0xffff0000, v16
	v_mul_f32_e32 v16, 0x3fb8aa3b, v46
	v_pk_mul_f32 v[42:43], v[68:69], v[42:43]
	v_exp_f32_e32 v68, v16
	v_mul_f32_e32 v16, 0x3fb8aa3b, v48
	v_exp_f32_e32 v69, v16
	v_and_b32_e32 v45, 0xffff0000, v20
	v_mul_f32_e32 v46, 0x3fb8aa3b, v47
	v_mul_f32_e32 v47, 0x3fb8aa3b, v49
	v_pk_mul_f32 v[44:45], v[70:71], v[44:45]
	v_rcp_f32_e32 v70, v68
	v_rcp_f32_e32 v71, v69
	v_exp_f32_e32 v46, v46
	v_exp_f32_e32 v47, v47
	v_lshlrev_b32_e32 v16, 16, v17
	v_and_b32_e32 v17, 0xffff0000, v17
	v_pk_mul_f32 v[34:35], v[72:73], v[34:35]
	v_pk_mul_f32 v[72:73], v[68:69], s[22:23] op_sel_hi:[1,0]
	v_pk_mul_f32 v[16:17], v[70:71], v[16:17]
	v_rcp_f32_e32 v68, v46
	v_pk_mul_f32 v[70:71], v[46:47], s[22:23] op_sel_hi:[1,0]
	v_rcp_f32_e32 v69, v47
	v_lshlrev_b32_e32 v46, 16, v18
	v_and_b32_e32 v47, 0xffff0000, v18
	v_mul_f32_e32 v18, 0x3fb8aa3b, v52
	v_exp_f32_e32 v52, v18
	v_mul_f32_e32 v18, 0x3fb8aa3b, v53
	v_exp_f32_e32 v53, v18
	v_pk_mul_f32 v[46:47], v[68:69], v[46:47]
	v_rcp_f32_e32 v68, v52
	v_lshlrev_b32_e32 v18, 16, v19
	v_rcp_f32_e32 v69, v53
	v_and_b32_e32 v19, 0xffff0000, v19
	v_lshlrev_b32_e32 v48, 16, v22
	v_and_b32_e32 v49, 0xffff0000, v22
	v_pk_mul_f32 v[18:19], v[68:69], v[18:19]
	v_rcp_f32_e32 v68, v50
	v_rcp_f32_e32 v69, v51
	v_pk_mul_f32 v[48:49], v[70:71], v[48:49]
	v_lshlrev_b32_e32 v22, 16, v23
	v_and_b32_e32 v23, 0xffff0000, v23
	v_pk_mul_f32 v[70:71], v[52:53], s[22:23] op_sel_hi:[1,0]
	v_lshlrev_b32_e32 v52, 16, v12
	v_pk_mul_f32 v[22:23], v[70:71], v[22:23]
	v_pk_mul_f32 v[70:71], v[50:51], s[22:23] op_sel_hi:[1,0]
	v_lshlrev_b32_e32 v50, 16, v8
	v_and_b32_e32 v51, 0xffff0000, v8
	v_mul_f32_e32 v8, 0x3fb8aa3b, v54
	v_pk_mul_f32 v[50:51], v[68:69], v[50:51]
	v_exp_f32_e32 v68, v8
	v_mul_f32_e32 v8, 0x3fb8aa3b, v56
	v_exp_f32_e32 v69, v8
	v_and_b32_e32 v53, 0xffff0000, v12
	v_mul_f32_e32 v54, 0x3fb8aa3b, v55
	v_mul_f32_e32 v55, 0x3fb8aa3b, v57
	v_pk_mul_f32 v[52:53], v[70:71], v[52:53]
	v_rcp_f32_e32 v70, v68
	v_rcp_f32_e32 v71, v69
	v_exp_f32_e32 v54, v54
	v_exp_f32_e32 v55, v55
	v_lshlrev_b32_e32 v20, 16, v21
	v_and_b32_e32 v21, 0xffff0000, v21
	v_lshlrev_b32_e32 v8, 16, v9
	v_and_b32_e32 v9, 0xffff0000, v9
	v_pk_mul_f32 v[20:21], v[72:73], v[20:21]
	v_pk_mul_f32 v[72:73], v[68:69], s[22:23] op_sel_hi:[1,0]
	v_pk_mul_f32 v[8:9], v[70:71], v[8:9]
	v_rcp_f32_e32 v68, v54
	v_pk_mul_f32 v[70:71], v[54:55], s[22:23] op_sel_hi:[1,0]
	v_rcp_f32_e32 v69, v55
	v_lshlrev_b32_e32 v54, 16, v10
	v_and_b32_e32 v55, 0xffff0000, v10
	v_mul_f32_e32 v10, 0x3fb8aa3b, v60
	v_exp_f32_e32 v60, v10
	v_mul_f32_e32 v10, 0x3fb8aa3b, v61
	v_exp_f32_e32 v61, v10
	v_pk_mul_f32 v[54:55], v[68:69], v[54:55]
	v_rcp_f32_e32 v68, v60
	v_lshlrev_b32_e32 v10, 16, v11
	v_rcp_f32_e32 v69, v61
	v_and_b32_e32 v11, 0xffff0000, v11
	v_lshlrev_b32_e32 v56, 16, v14
	v_and_b32_e32 v57, 0xffff0000, v14
	v_pk_mul_f32 v[10:11], v[68:69], v[10:11]
	v_rcp_f32_e32 v68, v58
	v_rcp_f32_e32 v69, v59
	v_pk_mul_f32 v[56:57], v[70:71], v[56:57]
	v_lshlrev_b32_e32 v14, 16, v15
	v_and_b32_e32 v15, 0xffff0000, v15
	v_pk_mul_f32 v[70:71], v[60:61], s[22:23] op_sel_hi:[1,0]
	v_lshlrev_b32_e32 v60, 16, v4
	v_pk_mul_f32 v[14:15], v[70:71], v[14:15]
	v_pk_mul_f32 v[70:71], v[58:59], s[22:23] op_sel_hi:[1,0]
	v_lshlrev_b32_e32 v58, 16, v0
	v_and_b32_e32 v59, 0xffff0000, v0
	v_mul_f32_e32 v0, 0x3fb8aa3b, v62
	v_pk_mul_f32 v[58:59], v[68:69], v[58:59]
	v_exp_f32_e32 v68, v0
	v_mul_f32_e32 v0, 0x3fb8aa3b, v65
	v_exp_f32_e32 v69, v0
	v_and_b32_e32 v61, 0xffff0000, v4
	v_pk_mul_f32 v[60:61], v[70:71], v[60:61]
	v_rcp_f32_e32 v4, v68
	v_lshlrev_b32_e32 v70, 16, v5
	v_and_b32_e32 v71, 0xffff0000, v5
	v_rcp_f32_e32 v5, v69
	v_lshlrev_b32_e32 v0, 16, v1
	v_and_b32_e32 v1, 0xffff0000, v1
	v_lshlrev_b32_e32 v12, 16, v13
	v_pk_mul_f32 v[4:5], v[4:5], v[0:1]
	v_mul_f32_e32 v0, 0x3fb8aa3b, v63
	v_mul_f32_e32 v1, 0x3fb8aa3b, v66
	v_exp_f32_e32 v0, v0
	v_exp_f32_e32 v1, v1
	v_and_b32_e32 v13, 0xffff0000, v13
	v_pk_mul_f32 v[12:13], v[72:73], v[12:13]
	v_rcp_f32_e32 v62, v0
	v_rcp_f32_e32 v63, v1
	v_pk_mul_f32 v[72:73], v[68:69], s[22:23] op_sel_hi:[1,0]
	v_lshlrev_b32_e32 v68, 16, v6
	v_pk_mul_f32 v[70:71], v[72:73], v[70:71]
	v_pk_mul_f32 v[72:73], v[0:1], s[22:23] op_sel_hi:[1,0]
	v_lshlrev_b32_e32 v0, 16, v2
	v_and_b32_e32 v1, 0xffff0000, v2
	v_pk_mul_f32 v[62:63], v[62:63], v[0:1]
	v_mul_f32_e32 v0, 0x3fb8aa3b, v64
	v_mul_f32_e32 v1, 0x3fb8aa3b, v67
	v_exp_f32_e32 v0, v0
	v_exp_f32_e32 v1, v1
	v_and_b32_e32 v69, 0xffff0000, v6
	v_lshlrev_b32_e32 v64, 16, v7
	v_rcp_f32_e32 v6, v0
	v_and_b32_e32 v65, 0xffff0000, v7
	v_rcp_f32_e32 v7, v1
	v_pk_mul_f32 v[66:67], v[0:1], s[22:23] op_sel_hi:[1,0]
	v_lshlrev_b32_e32 v0, 16, v3
	v_and_b32_e32 v1, 0xffff0000, v3
	v_pk_mul_f32 v[6:7], v[6:7], v[0:1]
	v_cvt_pk_bf16_f32 v0, v32, v33
	v_cvt_pk_bf16_f32 v1, v34, v35
	v_cvt_pk_bf16_f32 v2, v38, v39
	v_cvt_pk_bf16_f32 v3, v40, v41
	ds_write_b128 v99, v[0:3]
	v_cvt_pk_bf16_f32 v0, v30, v31
	v_cvt_pk_bf16_f32 v1, v24, v25
	v_cvt_pk_bf16_f32 v2, v36, v37
	v_cvt_pk_bf16_f32 v3, v26, v27
	ds_write_b128 v99, v[0:3] offset:4096
	v_cvt_pk_bf16_f32 v0, v44, v45
	v_cvt_pk_bf16_f32 v1, v20, v21
	v_cvt_pk_bf16_f32 v2, v48, v49
	v_cvt_pk_bf16_f32 v3, v22, v23
	ds_write_b128 v99, v[0:3] offset:16
	v_cvt_pk_bf16_f32 v0, v42, v43
	v_cvt_pk_bf16_f32 v1, v16, v17
	v_cvt_pk_bf16_f32 v2, v46, v47
	v_cvt_pk_bf16_f32 v3, v18, v19
	ds_write_b128 v99, v[0:3] offset:4112
	v_cvt_pk_bf16_f32 v0, v52, v53
	v_cvt_pk_bf16_f32 v1, v12, v13
	v_cvt_pk_bf16_f32 v2, v56, v57
	v_cvt_pk_bf16_f32 v3, v14, v15
	v_pk_mul_f32 v[68:69], v[72:73], v[68:69]
	v_pk_mul_f32 v[64:65], v[66:67], v[64:65]
	ds_write_b128 v99, v[0:3] offset:32
	v_cvt_pk_bf16_f32 v0, v50, v51
	v_cvt_pk_bf16_f32 v1, v8, v9
	v_cvt_pk_bf16_f32 v2, v54, v55
	v_cvt_pk_bf16_f32 v3, v10, v11
	ds_write_b128 v99, v[0:3] offset:4128
	v_cvt_pk_bf16_f32 v0, v60, v61
	v_cvt_pk_bf16_f32 v1, v70, v71
	v_cvt_pk_bf16_f32 v2, v68, v69
	v_cvt_pk_bf16_f32 v3, v64, v65
	ds_write_b128 v99, v[0:3] offset:48
	v_cvt_pk_bf16_f32 v0, v58, v59
	v_cvt_pk_bf16_f32 v1, v4, v5
	v_cvt_pk_bf16_f32 v2, v62, v63
	v_cvt_pk_bf16_f32 v3, v6, v7
	ds_write_b128 v99, v[0:3] offset:4144
	global_load_dwordx4 v[0:3], v[28:29], off offset:48
	global_load_dwordx4 v[4:7], v[28:29], off offset:32
	global_load_dwordx4 v[8:11], v[28:29], off offset:16
	global_load_dwordx4 v[12:15], v[28:29], off
	global_load_dwordx4 v[16:19], v[28:29], off offset:112
	global_load_dwordx4 v[20:23], v[28:29], off offset:96
	global_load_dwordx4 v[24:27], v[28:29], off offset:80
	s_nop 0
	global_load_dwordx4 v[28:31], v[28:29], off offset:64
	s_waitcnt vmcnt(0)
	ds_write_b16 v103, v12 offset:8192
	ds_write_b16_d16_hi v103, v12 offset:8320
	ds_write_b16 v103, v13 offset:8448
	ds_write_b16_d16_hi v103, v13 offset:8576
	ds_write_b16 v103, v14 offset:8704
	ds_write_b16_d16_hi v103, v14 offset:8832
	ds_write_b16 v103, v15 offset:8960
	ds_write_b16_d16_hi v103, v15 offset:9088
	ds_write_b16 v103, v8 offset:9216
	ds_write_b16_d16_hi v103, v8 offset:9344
	ds_write_b16 v103, v9 offset:9472
	ds_write_b16_d16_hi v103, v9 offset:9600
	ds_write_b16 v103, v10 offset:9728
	ds_write_b16_d16_hi v103, v10 offset:9856
	ds_write_b16 v103, v11 offset:9984
	ds_write_b16_d16_hi v103, v11 offset:10112
	ds_write_b16 v103, v4 offset:10240
	ds_write_b16_d16_hi v103, v4 offset:10368
	ds_write_b16 v103, v5 offset:10496
	ds_write_b16_d16_hi v103, v5 offset:10624
	ds_write_b16 v103, v6 offset:10752
	ds_write_b16_d16_hi v103, v6 offset:10880
	ds_write_b16 v103, v7 offset:11008
	ds_write_b16_d16_hi v103, v7 offset:11136
	ds_write_b16 v103, v0 offset:11264
	ds_write_b16_d16_hi v103, v0 offset:11392
	ds_write_b16 v103, v1 offset:11520
	ds_write_b16_d16_hi v103, v1 offset:11648
	ds_write_b16 v103, v2 offset:11776
	ds_write_b16_d16_hi v103, v2 offset:11904
	ds_write_b16 v103, v3 offset:12032
	ds_write_b16_d16_hi v103, v3 offset:12160
	ds_write_b16 v103, v28 offset:12288
	ds_write_b16_d16_hi v103, v28 offset:12416
	ds_write_b16 v103, v29 offset:12544
	ds_write_b16_d16_hi v103, v29 offset:12672
	ds_write_b16 v103, v30 offset:12800
	ds_write_b16_d16_hi v103, v30 offset:12928
	ds_write_b16 v103, v31 offset:13056
	ds_write_b16_d16_hi v103, v31 offset:13184
	ds_write_b16 v103, v24 offset:13312
	ds_write_b16_d16_hi v103, v24 offset:13440
	ds_write_b16 v103, v25 offset:13568
	ds_write_b16_d16_hi v103, v25 offset:13696
	ds_write_b16 v103, v26 offset:13824
	ds_write_b16_d16_hi v103, v26 offset:13952
	ds_write_b16 v103, v27 offset:14080
	ds_write_b16_d16_hi v103, v27 offset:14208
	ds_write_b16 v103, v20 offset:14336
	ds_write_b16_d16_hi v103, v20 offset:14464
	ds_write_b16 v103, v21 offset:14592
	ds_write_b16_d16_hi v103, v21 offset:14720
	ds_write_b16 v103, v22 offset:14848
	ds_write_b16_d16_hi v103, v22 offset:14976
	ds_write_b16 v103, v23 offset:15104
	ds_write_b16_d16_hi v103, v23 offset:15232
	ds_write_b16 v103, v16 offset:15360
	ds_write_b16_d16_hi v103, v16 offset:15488
	ds_write_b16 v103, v17 offset:15616
	ds_write_b16_d16_hi v103, v17 offset:15744
	ds_write_b16 v103, v18 offset:15872
	ds_write_b16_d16_hi v103, v18 offset:16000
	ds_write_b16 v103, v19 offset:16128
	ds_write_b16_d16_hi v103, v19 offset:16256
	s_waitcnt lgkmcnt(0)
	ds_read_b128 v[0:3], v148 offset:4096
	ds_read_b128 v[72:75], v148
	ds_read_b128 v[64:67], v148 offset:32
	ds_read_b128 v[48:51], v148 offset:4128
	ds_read_b128 v[76:79], v148 offset:2048
	ds_read_b128 v[32:35], v148 offset:6144
	ds_read_b128 v[68:71], v148 offset:2080
	ds_read_b128 v[52:55], v148 offset:6176
	s_waitcnt lgkmcnt(6)
	v_mfma_f32_32x32x16_bf16 v[16:31], v[0:3], v[72:75], 0
	s_waitcnt lgkmcnt(3)
	v_mfma_f32_32x32x16_bf16 v[0:15], v[0:3], v[76:79], 0
	s_waitcnt lgkmcnt(1)
	v_mfma_f32_32x32x16_bf16 v[0:15], v[48:51], v[68:71], v[0:15]
	v_mfma_f32_32x32x16_bf16 v[32:47], v[32:35], v[76:79], 0
	s_nop 10
	v_cvt_pk_bf16_f32 v86, v12, v13
	v_add_u32_e32 v12, 0x2000, v149
	v_cvt_pk_bf16_f32 v0, v0, v1
	v_cvt_pk_bf16_f32 v1, v2, v3
	v_cvt_pk_bf16_f32 v2, v4, v5
	v_cvt_pk_bf16_f32 v3, v6, v7
	v_cvt_pk_bf16_f32 v84, v8, v9
	v_mfma_f32_32x32x16_bf16 v[16:31], v[48:51], v[64:67], v[16:31]
	v_cvt_pk_bf16_f32 v85, v10, v11
	ds_read2_b64 v[4:7], v12 offset1:2
	ds_read2_b64 v[8:11], v12 offset0:4 offset1:6
	v_cvt_pk_bf16_f32 v87, v14, v15
	s_waitcnt lgkmcnt(2)
	v_mfma_f32_32x32x16_bf16 v[32:47], v[52:55], v[68:71], v[32:47]
	s_nop 5
	v_cndmask_b32_e64 v16, v16, 0, s[48:49]
	v_cndmask_b32_e64 v17, 0, v17, s[50:51]
	v_cndmask_b32_e64 v18, v18, 0, s[52:53]
	v_cndmask_b32_e64 v19, v19, 0, s[54:55]
	v_cndmask_b32_e64 v20, v20, 0, s[56:57]
	v_cndmask_b32_e64 v21, v21, 0, s[58:59]
	v_cndmask_b32_e64 v22, v22, 0, s[60:61]
	v_cndmask_b32_e64 v23, v23, 0, s[62:63]
	v_cndmask_b32_e64 v24, v24, 0, s[64:65]
	v_cndmask_b32_e64 v25, v25, 0, s[66:67]
	v_cndmask_b32_e64 v26, v26, 0, s[68:69]
	v_cndmask_b32_e64 v27, v27, 0, s[70:71]
	v_cndmask_b32_e64 v28, v28, 0, s[72:73]
	v_cndmask_b32_e64 v29, v29, 0, s[74:75]
	v_cndmask_b32_e64 v30, v30, 0, s[76:77]
	v_cndmask_b32_e64 v31, v31, 0, s[78:79]
	v_cvt_pk_bf16_f32 v48, v16, v17
	v_cvt_pk_bf16_f32 v49, v18, v19
	v_cvt_pk_bf16_f32 v50, v20, v21
	v_cvt_pk_bf16_f32 v51, v22, v23
	v_cvt_pk_bf16_f32 v80, v24, v25
	v_cvt_pk_bf16_f32 v81, v26, v27
	v_cvt_pk_bf16_f32 v82, v28, v29
	v_cvt_pk_bf16_f32 v83, v30, v31
	s_waitcnt lgkmcnt(1)
	v_mfma_f32_32x32x16_bf16 v[16:31], v[4:7], v[0:3], 0
	v_cndmask_b32_e64 v32, v32, 0, s[48:49]
	v_cndmask_b32_e64 v33, 0, v33, s[50:51]
	v_cndmask_b32_e64 v34, v34, 0, s[52:53]
	v_cndmask_b32_e64 v35, v35, 0, s[54:55]
	v_cndmask_b32_e64 v36, v36, 0, s[56:57]
	v_cndmask_b32_e64 v37, v37, 0, s[58:59]
	v_cndmask_b32_e64 v38, v38, 0, s[60:61]
	v_cndmask_b32_e64 v39, v39, 0, s[62:63]
	v_cndmask_b32_e64 v40, v40, 0, s[64:65]
	v_cndmask_b32_e64 v41, v41, 0, s[66:67]
	v_cndmask_b32_e64 v42, v42, 0, s[68:69]
	v_cndmask_b32_e64 v43, v43, 0, s[70:71]
	v_cndmask_b32_e64 v44, v44, 0, s[72:73]
	v_cndmask_b32_e64 v45, v45, 0, s[74:75]
	v_cndmask_b32_e64 v46, v46, 0, s[76:77]
	v_cndmask_b32_e64 v47, v47, 0, s[78:79]
	v_cvt_pk_bf16_f32 v88, v32, v33
	v_cvt_pk_bf16_f32 v89, v34, v35
	v_cvt_pk_bf16_f32 v90, v36, v37
	v_cvt_pk_bf16_f32 v91, v38, v39
	v_cvt_pk_bf16_f32 v92, v40, v41
	v_cvt_pk_bf16_f32 v93, v42, v43
	v_cvt_pk_bf16_f32 v94, v44, v45
	v_cvt_pk_bf16_f32 v95, v46, v47
	v_mfma_f32_32x32x16_bf16 v[32:47], v[4:7], v[48:51], 0
	ds_read2_b64 v[4:7], v12 offset0:8 offset1:10
	s_waitcnt lgkmcnt(1)
	v_mfma_f32_32x32x16_bf16 v[16:31], v[8:11], v[84:87], v[16:31]
	s_waitcnt lgkmcnt(0)
	v_mfma_f32_32x32x16_bf16 v[16:31], v[4:7], v[88:91], v[16:31]
	ds_read2_b64 v[4:7], v12 offset0:12 offset1:14
	s_waitcnt lgkmcnt(0)
	v_mfma_f32_32x32x16_bf16 v[16:31], v[4:7], v[92:95], v[16:31]
	v_lshl_add_u64 v[4:5], s[12:13], 0, v[136:137]
	global_load_dword v6, v[4:5], off
	v_lshl_add_u64 v[4:5], s[12:13], 0, v[128:129]
	v_mfma_f32_32x32x16_bf16 v[32:47], v[8:11], v[80:83], v[32:47]
	global_load_dword v7, v[4:5], off offset:-768
	global_load_dword v8, v[4:5], off offset:-512
	global_load_dword v9, v[4:5], off offset:-256
	global_load_dword v10, v[4:5], off
	global_load_dword v11, v[4:5], off offset:256
	global_load_dword v12, v[4:5], off offset:512
	global_load_dword v13, v[4:5], off offset:768
	ds_read2_b64 v[150:153], v154 offset0:4 offset1:6
	s_waitcnt vmcnt(6)
	v_cvt_pk_bf16_f32 v4, v6, v7
	s_waitcnt vmcnt(4)
	v_cvt_pk_bf16_f32 v5, v8, v9
	s_waitcnt vmcnt(2)
	v_cvt_pk_bf16_f32 v6, v10, v11
	s_waitcnt vmcnt(0)
	v_cvt_pk_bf16_f32 v7, v12, v13
	s_nop 1
	v_mfma_f32_32x32x16_bf16 v[32:47], v[4:7], v[72:75], v[32:47]
	v_mfma_f32_32x32x16_bf16 v[16:31], v[4:7], v[76:79], v[16:31]
	v_lshl_add_u64 v[4:5], s[12:13], 0, v[138:139]
	global_load_dword v6, v[4:5], off
	v_lshl_add_u64 v[4:5], s[12:13], 0, v[140:141]
	global_load_dword v7, v[4:5], off
	v_lshl_add_u64 v[4:5], s[12:13], 0, v[142:143]
	global_load_dword v8, v[4:5], off
	v_lshl_add_u64 v[4:5], s[12:13], 0, v[144:145]
	global_load_dword v9, v[4:5], off
	v_lshl_add_u64 v[4:5], s[12:13], 0, v[146:147]
	global_load_dword v10, v[4:5], off
	v_lshl_add_u64 v[4:5], s[12:13], 0, v[134:135]
	global_load_dword v11, v[4:5], off
	v_lshl_add_u64 v[4:5], s[12:13], 0, v[132:133]
	global_load_dword v12, v[4:5], off
	v_lshl_add_u64 v[4:5], s[12:13], 0, v[130:131]
	global_load_dword v13, v[4:5], off
	s_waitcnt vmcnt(6)
	v_cvt_pk_bf16_f32 v4, v6, v7
	s_waitcnt vmcnt(4)
	v_cvt_pk_bf16_f32 v5, v8, v9
	s_waitcnt vmcnt(2)
	v_cvt_pk_bf16_f32 v6, v10, v11
	s_waitcnt vmcnt(0)
	v_cvt_pk_bf16_f32 v7, v12, v13
	s_nop 1
	v_mfma_f32_32x32x16_bf16 v[32:47], v[4:7], v[64:67], v[32:47]
	v_mfma_f32_32x32x16_bf16 v[16:31], v[4:7], v[68:71], v[16:31]
	ds_read2_b64 v[4:7], v154 offset1:2
	s_waitcnt lgkmcnt(0)
	v_mfma_f32_32x32x16_bf16 v[48:63], v[4:7], v[48:51], 0
	v_mfma_f32_32x32x16_bf16 v[0:15], v[4:7], v[0:3], 0
	v_mfma_f32_32x32x16_bf16 v[48:63], v[150:153], v[80:83], v[48:63]
	ds_read2_b64 v[80:83], v154 offset0:8 offset1:10
	v_mfma_f32_32x32x16_bf16 v[0:15], v[150:153], v[84:87], v[0:15]
	s_waitcnt lgkmcnt(0)
	v_mfma_f32_32x32x16_bf16 v[0:15], v[80:83], v[88:91], v[0:15]
	ds_read2_b64 v[80:83], v154 offset0:12 offset1:14
	s_waitcnt lgkmcnt(0)
	v_mfma_f32_32x32x16_bf16 v[0:15], v[80:83], v[92:95], v[0:15]
	v_lshl_add_u64 v[80:81], s[12:13], 0, v[126:127]
	global_load_dword v82, v[80:81], off
	v_lshl_add_u64 v[80:81], s[12:13], 0, v[114:115]
	global_load_dword v83, v[80:81], off offset:-768
	global_load_dword v84, v[80:81], off offset:-512
	global_load_dword v85, v[80:81], off offset:-256
	global_load_dword v86, v[80:81], off
	global_load_dword v87, v[80:81], off offset:256
	global_load_dword v88, v[80:81], off offset:512
	global_load_dword v89, v[80:81], off offset:768
	s_waitcnt vmcnt(4)
	v_cvt_pk_bf16_f32 v81, v84, v85
	v_cvt_pk_bf16_f32 v80, v82, v83
	s_waitcnt vmcnt(2)
	v_cvt_pk_bf16_f32 v82, v86, v87
	s_waitcnt vmcnt(0)
	v_cvt_pk_bf16_f32 v83, v88, v89
	s_nop 1
	v_mfma_f32_32x32x16_bf16 v[48:63], v[80:83], v[72:75], v[48:63]
	v_lshl_add_u64 v[72:73], s[12:13], 0, v[124:125]
	global_load_dword v74, v[72:73], off
	v_lshl_add_u64 v[72:73], s[12:13], 0, v[122:123]
	global_load_dword v75, v[72:73], off
	v_lshl_add_u64 v[72:73], s[12:13], 0, v[120:121]
	v_mfma_f32_32x32x16_bf16 v[0:15], v[80:83], v[76:79], v[0:15]
	global_load_dword v76, v[72:73], off
	v_lshl_add_u64 v[72:73], s[12:13], 0, v[118:119]
	global_load_dword v77, v[72:73], off
	v_lshl_add_u64 v[72:73], s[12:13], 0, v[116:117]
	global_load_dword v78, v[72:73], off
	v_lshl_add_u64 v[72:73], s[12:13], 0, v[112:113]
	global_load_dword v79, v[72:73], off
	v_lshl_add_u64 v[72:73], s[12:13], 0, v[110:111]
	global_load_dword v80, v[72:73], off
	v_lshl_add_u64 v[72:73], s[12:13], 0, v[96:97]
	global_load_dword v81, v[72:73], off
	s_add_u32 s12, s12, s20
	s_addc_u32 s13, s13, s21
	s_cmpk_gt_i32 s16, 0x3ff
	s_waitcnt vmcnt(6)
	v_cvt_pk_bf16_f32 v72, v74, v75
	s_waitcnt vmcnt(4)
	v_cvt_pk_bf16_f32 v73, v76, v77
	s_waitcnt vmcnt(2)
	v_cvt_pk_bf16_f32 v74, v78, v79
	s_waitcnt vmcnt(0)
	v_cvt_pk_bf16_f32 v75, v80, v81
	s_nop 1
	v_mfma_f32_32x32x16_bf16 v[48:63], v[72:75], v[64:67], v[48:63]
	v_mul_f32_e32 v66, v33, v33
	v_fmac_f32_e32 v66, v32, v32
	v_fmac_f32_e32 v66, v34, v34
	v_fmac_f32_e32 v66, v35, v35
	v_fmac_f32_e32 v66, v36, v36
	v_fmac_f32_e32 v66, v37, v37
	v_fmac_f32_e32 v66, v38, v38
	v_fmac_f32_e32 v66, v39, v39
	v_fmac_f32_e32 v66, v40, v40
	v_fmac_f32_e32 v66, v41, v41
	v_fmac_f32_e32 v66, v42, v42
	v_fmac_f32_e32 v66, v43, v43
	v_fmac_f32_e32 v66, v44, v44
	v_fmac_f32_e32 v66, v45, v45
	v_fmac_f32_e32 v66, v46, v46
	v_fmac_f32_e32 v66, v47, v47
	v_fmac_f32_e32 v66, v48, v48
	v_fmac_f32_e32 v66, v49, v49
	v_fmac_f32_e32 v66, v50, v50
	v_fmac_f32_e32 v66, v51, v51
	v_fmac_f32_e32 v66, v52, v52
	v_fmac_f32_e32 v66, v53, v53
	v_fmac_f32_e32 v66, v54, v54
	v_fmac_f32_e32 v66, v55, v55
	v_fmac_f32_e32 v66, v56, v56
	v_fmac_f32_e32 v66, v57, v57
	v_fmac_f32_e32 v66, v58, v58
	v_fmac_f32_e32 v66, v59, v59
	v_fmac_f32_e32 v66, v60, v60
	v_fmac_f32_e32 v66, v61, v61
	v_pk_mul_f32 v[64:65], v[62:63], v[62:63]
	v_mfma_f32_32x32x16_bf16 v[0:15], v[72:75], v[68:71], v[0:15]
	v_add_f32_e32 v64, v64, v66
	v_add_f32_e32 v64, v65, v64
	v_mov_b32_e32 v65, v64
	s_nop 1
	v_permlane32_swap_b32_e32 v64, v65
	v_add_f32_e32 v64, v64, v65
	v_fmamk_f32 v64, v64, 0x3c800000, v241
	v_cmp_gt_f32_e32 vcc, s1, v64
	v_mul_f32_e32 v65, 0x4f800000, v64
	v_mov_b32_e32 v71, s15
	v_cndmask_b32_e32 v64, v64, v65, vcc
	v_sqrt_f32_e32 v65, v64
	v_or_b32_e32 v70, s14, v198
	v_add_u32_e32 v66, -1, v65
	v_fma_f32 v67, -v66, v65, v64
	v_cmp_ge_f32_e64 s[2:3], 0, v67
	v_add_u32_e32 v67, 1, v65
	s_nop 0
	v_cndmask_b32_e64 v66, v65, v66, s[2:3]
	v_fma_f32 v65, -v67, v65, v64
	v_cmp_lt_f32_e64 s[2:3], 0, v65
	s_nop 1
	v_cndmask_b32_e64 v65, v66, v67, s[2:3]
	v_mul_f32_e32 v66, 0x37800000, v65
	v_cndmask_b32_e32 v65, v65, v66, vcc
	v_cmp_class_f32_e32 vcc, v64, v240
	s_nop 1
	v_cndmask_b32_e32 v64, v65, v64, vcc
	v_div_scale_f32 v65, s[2:3], v64, v64, 1.0
	v_rcp_f32_e32 v66, v65
	s_nop 0
	v_fma_f32 v67, -v65, v66, 1.0
	v_fmac_f32_e32 v66, v67, v66
	v_div_scale_f32 v67, vcc, 1.0, v64, 1.0
	v_mul_f32_e32 v68, v67, v66
	v_fma_f32 v69, -v65, v68, v67
	v_fmac_f32_e32 v68, v69, v66
	v_fma_f32 v65, -v65, v68, v67
	v_div_fmas_f32 v65, v65, v66, v68
	v_lshlrev_b64 v[66:67], 9, v[70:71]
	v_lshl_add_u64 v[72:73], v[106:107], 0, v[66:67]
	global_load_dwordx2 v[74:75], v[72:73], off
	global_load_dwordx4 v[66:69], v[104:105], off
	v_div_fixup_f32 v64, v65, v64, 1.0
	s_waitcnt vmcnt(1)
	v_lshlrev_b32_e32 v76, 16, v74
	v_mul_f32_e32 v65, 0xbfb8aa3b, v76
	v_exp_f32_e32 v65, v65
	v_and_b32_e32 v77, 0xffff0000, v74
	v_add_f32_e32 v65, 1.0, v65
	v_rcp_f32_e32 v78, v65
	v_pk_mul_f32 v[32:33], v[32:33], v[64:65] op_sel_hi:[1,0]
	v_mul_f32_e32 v65, 0xbfb8aa3b, v77
	v_exp_f32_e32 v65, v65
	s_waitcnt vmcnt(0)
	v_pk_mul_f32 v[32:33], v[66:67], v[32:33]
	v_add_f32_e32 v65, 1.0, v65
	v_rcp_f32_e32 v79, v65
	s_nop 0
	v_pk_mul_f32 v[66:67], v[78:79], v[76:77]
	s_nop 0
	v_pk_mul_f32 v[32:33], v[32:33], v[66:67]
	v_lshlrev_b32_e32 v66, 16, v75
	v_mul_f32_e32 v65, 0xbfb8aa3b, v66
	v_exp_f32_e32 v65, v65
	v_and_b32_e32 v67, 0xffff0000, v75
	v_cvt_pk_bf16_f32 v32, v32, v33
	v_add_f32_e32 v65, 1.0, v65
	v_rcp_f32_e32 v74, v65
	v_pk_mul_f32 v[34:35], v[34:35], v[64:65] op_sel_hi:[1,0]
	v_mul_f32_e32 v65, 0xbfb8aa3b, v67
	v_exp_f32_e32 v65, v65
	v_pk_mul_f32 v[34:35], v[68:69], v[34:35]
	v_add_f32_e32 v65, 1.0, v65
	v_rcp_f32_e32 v75, v65
	s_nop 0
	v_pk_mul_f32 v[66:67], v[74:75], v[66:67]
	s_nop 0
	v_pk_mul_f32 v[34:35], v[34:35], v[66:67]
	v_mad_u64_u32 v[66:67], s[2:3], v70, s83, v[108:109]
	v_cvt_pk_bf16_f32 v33, v34, v35
	v_mad_i32_i24 v67, s15, v227, v67
	global_store_dwordx2 v[66:67], v[32:33], off
	global_load_dwordx2 v[68:69], v[72:73], off offset:16
	s_nop 0
	global_load_dwordx4 v[32:35], v[104:105], off offset:32
	s_waitcnt vmcnt(1)
	v_lshlrev_b32_e32 v70, 16, v68
	v_mul_f32_e32 v65, 0xbfb8aa3b, v70
	v_exp_f32_e32 v65, v65
	v_and_b32_e32 v71, 0xffff0000, v68
	v_add_f32_e32 v65, 1.0, v65
	v_pk_mul_f32 v[36:37], v[36:37], v[64:65] op_sel_hi:[1,0]
	v_rcp_f32_e32 v74, v65
	s_waitcnt vmcnt(0)
	v_pk_mul_f32 v[32:33], v[32:33], v[36:37]
	v_mul_f32_e32 v36, 0xbfb8aa3b, v71
	v_exp_f32_e32 v36, v36
	s_nop 0
	v_add_f32_e32 v36, 1.0, v36
	v_rcp_f32_e32 v75, v36
	s_nop 0
	v_pk_mul_f32 v[36:37], v[74:75], v[70:71]
	s_nop 0
	v_pk_mul_f32 v[32:33], v[32:33], v[36:37]
	v_lshlrev_b32_e32 v36, 16, v69
	v_mul_f32_e32 v65, 0xbfb8aa3b, v36
	v_exp_f32_e32 v65, v65
	v_and_b32_e32 v37, 0xffff0000, v69
	v_cvt_pk_bf16_f32 v32, v32, v33
	v_add_f32_e32 v65, 1.0, v65
	v_pk_mul_f32 v[38:39], v[38:39], v[64:65] op_sel_hi:[1,0]
	v_rcp_f32_e32 v68, v65
	v_pk_mul_f32 v[34:35], v[34:35], v[38:39]
	v_mul_f32_e32 v38, 0xbfb8aa3b, v37
	v_exp_f32_e32 v38, v38
	v_pk_mul_f32 v[40:41], v[40:41], v[64:65] op_sel_hi:[1,0]
	v_add_f32_e32 v38, 1.0, v38
	v_rcp_f32_e32 v69, v38
	s_nop 0
	v_pk_mul_f32 v[36:37], v[68:69], v[36:37]
	s_nop 0
	v_pk_mul_f32 v[34:35], v[34:35], v[36:37]
	s_nop 0
	v_cvt_pk_bf16_f32 v33, v34, v35
	global_store_dwordx2 v[66:67], v[32:33], off offset:16
	global_load_dwordx2 v[36:37], v[72:73], off offset:32
	s_nop 0
	global_load_dwordx4 v[32:35], v[104:105], off offset:64
	s_waitcnt vmcnt(1)
	v_lshlrev_b32_e32 v38, 16, v36
	v_and_b32_e32 v39, 0xffff0000, v36
	v_mul_f32_e32 v36, 0xbfb8aa3b, v38
	v_exp_f32_e32 v36, v36
	s_waitcnt vmcnt(0)
	v_pk_mul_f32 v[32:33], v[40:41], v[32:33]
	v_pk_mul_f32 v[40:41], v[42:43], v[64:65] op_sel_hi:[1,0]
	v_pk_mul_f32 v[42:43], v[44:45], v[64:65] op_sel_hi:[1,0]
	v_add_f32_e32 v36, 1.0, v36
	v_rcp_f32_e32 v68, v36
	v_mul_f32_e32 v36, 0xbfb8aa3b, v39
	v_exp_f32_e32 v36, v36
	v_pk_mul_f32 v[34:35], v[40:41], v[34:35]
	v_add_f32_e32 v36, 1.0, v36
	v_rcp_f32_e32 v69, v36
	v_lshlrev_b32_e32 v36, 16, v37
	v_and_b32_e32 v37, 0xffff0000, v37
	v_pk_mul_f32 v[38:39], v[68:69], v[38:39]
	s_nop 0
	v_pk_mul_f32 v[32:33], v[32:33], v[38:39]
	v_mul_f32_e32 v38, 0xbfb8aa3b, v36
	v_mul_f32_e32 v39, 0xbfb8aa3b, v37
	v_exp_f32_e32 v38, v38
	v_exp_f32_e32 v39, v39
	v_cvt_pk_bf16_f32 v32, v32, v33
	v_add_f32_e32 v38, 1.0, v38
	v_add_f32_e32 v39, 1.0, v39
	v_rcp_f32_e32 v38, v38
	v_rcp_f32_e32 v39, v39
	s_nop 0
	v_pk_mul_f32 v[36:37], v[38:39], v[36:37]
	s_nop 0
	v_pk_mul_f32 v[34:35], v[34:35], v[36:37]
	s_nop 0
	v_cvt_pk_bf16_f32 v33, v34, v35
	global_store_dwordx2 v[66:67], v[32:33], off offset:32
	global_load_dwordx2 v[36:37], v[72:73], off offset:48
	s_nop 0
	global_load_dwordx4 v[32:35], v[104:105], off offset:96
	s_waitcnt vmcnt(1)
	v_lshlrev_b32_e32 v38, 16, v36
	v_and_b32_e32 v39, 0xffff0000, v36
	v_mul_f32_e32 v36, 0xbfb8aa3b, v38
	v_exp_f32_e32 v36, v36
	s_waitcnt vmcnt(0)
	v_pk_mul_f32 v[32:33], v[42:43], v[32:33]
	v_pk_mul_f32 v[42:43], v[48:49], v[64:65] op_sel_hi:[1,0]
	v_add_f32_e32 v36, 1.0, v36
	v_rcp_f32_e32 v40, v36
	v_mul_f32_e32 v36, 0xbfb8aa3b, v39
	v_exp_f32_e32 v36, v36
	s_nop 0
	v_add_f32_e32 v36, 1.0, v36
	v_rcp_f32_e32 v41, v36
	v_lshlrev_b32_e32 v36, 16, v37
	v_and_b32_e32 v37, 0xffff0000, v37
	v_pk_mul_f32 v[38:39], v[40:41], v[38:39]
	s_nop 0
	v_pk_mul_f32 v[32:33], v[32:33], v[38:39]
	v_mul_f32_e32 v38, 0xbfb8aa3b, v36
	v_mul_f32_e32 v39, 0xbfb8aa3b, v37
	v_exp_f32_e32 v38, v38
	v_exp_f32_e32 v39, v39
	v_pk_mul_f32 v[40:41], v[46:47], v[64:65] op_sel_hi:[1,0]
	v_cvt_pk_bf16_f32 v32, v32, v33
	v_add_f32_e32 v38, 1.0, v38
	v_add_f32_e32 v39, 1.0, v39
	v_rcp_f32_e32 v38, v38
	v_rcp_f32_e32 v39, v39
	v_pk_mul_f32 v[34:35], v[40:41], v[34:35]
	v_pk_mul_f32 v[36:37], v[38:39], v[36:37]
	s_nop 0
	v_pk_mul_f32 v[34:35], v[34:35], v[36:37]
	s_nop 0
	v_cvt_pk_bf16_f32 v33, v34, v35
	global_store_dwordx2 v[66:67], v[32:33], off offset:48
	global_load_dwordx2 v[36:37], v[72:73], off offset:64
	s_nop 0
	global_load_dwordx4 v[32:35], v[104:105], off offset:128
	s_waitcnt vmcnt(1)
	v_lshlrev_b32_e32 v38, 16, v36
	v_and_b32_e32 v39, 0xffff0000, v36
	v_mul_f32_e32 v36, 0xbfb8aa3b, v38
	v_exp_f32_e32 v36, v36
	s_waitcnt vmcnt(0)
	v_pk_mul_f32 v[32:33], v[42:43], v[32:33]
	v_pk_mul_f32 v[42:43], v[52:53], v[64:65] op_sel_hi:[1,0]
	v_add_f32_e32 v36, 1.0, v36
	v_rcp_f32_e32 v40, v36
	v_mul_f32_e32 v36, 0xbfb8aa3b, v39
	v_exp_f32_e32 v36, v36
	s_nop 0
	v_add_f32_e32 v36, 1.0, v36
	v_rcp_f32_e32 v41, v36
	v_lshlrev_b32_e32 v36, 16, v37
	v_and_b32_e32 v37, 0xffff0000, v37
	v_pk_mul_f32 v[38:39], v[40:41], v[38:39]
	s_nop 0
	v_pk_mul_f32 v[32:33], v[32:33], v[38:39]
	v_mul_f32_e32 v38, 0xbfb8aa3b, v36
	v_mul_f32_e32 v39, 0xbfb8aa3b, v37
	v_exp_f32_e32 v38, v38
	v_exp_f32_e32 v39, v39
	v_pk_mul_f32 v[40:41], v[50:51], v[64:65] op_sel_hi:[1,0]
	v_cvt_pk_bf16_f32 v32, v32, v33
	v_add_f32_e32 v38, 1.0, v38
	v_add_f32_e32 v39, 1.0, v39
	v_rcp_f32_e32 v38, v38
	v_rcp_f32_e32 v39, v39
	v_pk_mul_f32 v[34:35], v[40:41], v[34:35]
	v_pk_mul_f32 v[36:37], v[38:39], v[36:37]
	s_nop 0
	v_pk_mul_f32 v[34:35], v[34:35], v[36:37]
	s_nop 0
	v_cvt_pk_bf16_f32 v33, v34, v35
	global_store_dwordx2 v[66:67], v[32:33], off offset:64
	global_load_dwordx2 v[36:37], v[72:73], off offset:80
	s_nop 0
	global_load_dwordx4 v[32:35], v[104:105], off offset:160
	s_waitcnt vmcnt(1)
	v_lshlrev_b32_e32 v38, 16, v36
	v_and_b32_e32 v39, 0xffff0000, v36
	v_mul_f32_e32 v36, 0xbfb8aa3b, v38
	v_exp_f32_e32 v36, v36
	s_waitcnt vmcnt(0)
	v_pk_mul_f32 v[32:33], v[42:43], v[32:33]
	v_pk_mul_f32 v[42:43], v[56:57], v[64:65] op_sel_hi:[1,0]
	v_add_f32_e32 v36, 1.0, v36
	v_rcp_f32_e32 v40, v36
	v_mul_f32_e32 v36, 0xbfb8aa3b, v39
	v_exp_f32_e32 v36, v36
	s_nop 0
	v_add_f32_e32 v36, 1.0, v36
	v_rcp_f32_e32 v41, v36
	v_lshlrev_b32_e32 v36, 16, v37
	v_and_b32_e32 v37, 0xffff0000, v37
	v_pk_mul_f32 v[38:39], v[40:41], v[38:39]
	s_nop 0
	v_pk_mul_f32 v[32:33], v[32:33], v[38:39]
	v_mul_f32_e32 v38, 0xbfb8aa3b, v36
	v_mul_f32_e32 v39, 0xbfb8aa3b, v37
	v_exp_f32_e32 v38, v38
	v_exp_f32_e32 v39, v39
	v_pk_mul_f32 v[40:41], v[54:55], v[64:65] op_sel_hi:[1,0]
	v_cvt_pk_bf16_f32 v32, v32, v33
	v_add_f32_e32 v38, 1.0, v38
	v_add_f32_e32 v39, 1.0, v39
	v_rcp_f32_e32 v38, v38
	v_rcp_f32_e32 v39, v39
	v_pk_mul_f32 v[34:35], v[40:41], v[34:35]
	v_pk_mul_f32 v[36:37], v[38:39], v[36:37]
	s_nop 0
	v_pk_mul_f32 v[34:35], v[34:35], v[36:37]
	s_nop 0
	v_cvt_pk_bf16_f32 v33, v34, v35
	global_store_dwordx2 v[66:67], v[32:33], off offset:80
	global_load_dwordx2 v[36:37], v[72:73], off offset:96
	s_nop 0
	global_load_dwordx4 v[32:35], v[104:105], off offset:192
	s_waitcnt vmcnt(1)
	v_lshlrev_b32_e32 v38, 16, v36
	v_and_b32_e32 v39, 0xffff0000, v36
	v_mul_f32_e32 v36, 0xbfb8aa3b, v38
	v_exp_f32_e32 v36, v36
	s_waitcnt vmcnt(0)
	v_pk_mul_f32 v[32:33], v[42:43], v[32:33]
	v_pk_mul_f32 v[42:43], v[60:61], v[64:65] op_sel_hi:[1,0]
	v_add_f32_e32 v36, 1.0, v36
	v_rcp_f32_e32 v40, v36
	v_mul_f32_e32 v36, 0xbfb8aa3b, v39
	v_exp_f32_e32 v36, v36
	s_nop 0
	v_add_f32_e32 v36, 1.0, v36
	v_rcp_f32_e32 v41, v36
	v_lshlrev_b32_e32 v36, 16, v37
	v_and_b32_e32 v37, 0xffff0000, v37
	v_pk_mul_f32 v[38:39], v[40:41], v[38:39]
	s_nop 0
	v_pk_mul_f32 v[32:33], v[32:33], v[38:39]
	v_mul_f32_e32 v38, 0xbfb8aa3b, v36
	v_mul_f32_e32 v39, 0xbfb8aa3b, v37
	v_exp_f32_e32 v38, v38
	v_exp_f32_e32 v39, v39
	v_pk_mul_f32 v[40:41], v[58:59], v[64:65] op_sel_hi:[1,0]
	v_cvt_pk_bf16_f32 v32, v32, v33
	v_add_f32_e32 v38, 1.0, v38
	v_add_f32_e32 v39, 1.0, v39
	v_rcp_f32_e32 v38, v38
	v_rcp_f32_e32 v39, v39
	v_pk_mul_f32 v[34:35], v[40:41], v[34:35]
	v_pk_mul_f32 v[36:37], v[38:39], v[36:37]
	s_nop 0
	v_pk_mul_f32 v[34:35], v[34:35], v[36:37]
	s_nop 0
	v_cvt_pk_bf16_f32 v33, v34, v35
	global_store_dwordx2 v[66:67], v[32:33], off offset:96
	global_load_dwordx2 v[36:37], v[72:73], off offset:112
	s_nop 0
	global_load_dwordx4 v[32:35], v[104:105], off offset:224
	s_waitcnt vmcnt(1)
	v_lshlrev_b32_e32 v38, 16, v36
	v_and_b32_e32 v39, 0xffff0000, v36
	v_mul_f32_e32 v36, 0xbfb8aa3b, v38
	v_exp_f32_e32 v36, v36
	s_waitcnt vmcnt(0)
	v_pk_mul_f32 v[32:33], v[42:43], v[32:33]
	v_add_f32_e32 v36, 1.0, v36
	v_rcp_f32_e32 v40, v36
	v_mul_f32_e32 v36, 0xbfb8aa3b, v39
	v_exp_f32_e32 v36, v36
	s_nop 0
	v_add_f32_e32 v36, 1.0, v36
	v_rcp_f32_e32 v41, v36
	v_lshlrev_b32_e32 v36, 16, v37
	v_and_b32_e32 v37, 0xffff0000, v37
	v_pk_mul_f32 v[38:39], v[40:41], v[38:39]
	s_nop 0
	v_pk_mul_f32 v[32:33], v[32:33], v[38:39]
	v_mul_f32_e32 v38, 0xbfb8aa3b, v36
	v_mul_f32_e32 v39, 0xbfb8aa3b, v37
	v_exp_f32_e32 v38, v38
	v_exp_f32_e32 v39, v39
	v_pk_mul_f32 v[40:41], v[62:63], v[64:65] op_sel_hi:[1,0]
	v_cvt_pk_bf16_f32 v32, v32, v33
	v_add_f32_e32 v38, 1.0, v38
	v_add_f32_e32 v39, 1.0, v39
	v_rcp_f32_e32 v38, v38
	v_rcp_f32_e32 v39, v39
	v_pk_mul_f32 v[34:35], v[40:41], v[34:35]
	v_mov_b32_e32 v41, s15
	v_or_b32_e32 v40, s14, v102
	v_pk_mul_f32 v[36:37], v[38:39], v[36:37]
	s_nop 0
	v_pk_mul_f32 v[34:35], v[34:35], v[36:37]
	s_nop 0
	v_cvt_pk_bf16_f32 v33, v34, v35
	v_mul_f32_e32 v34, v17, v17
	v_fmac_f32_e32 v34, v16, v16
	v_fmac_f32_e32 v34, v18, v18
	v_fmac_f32_e32 v34, v19, v19
	v_fmac_f32_e32 v34, v20, v20
	v_fmac_f32_e32 v34, v21, v21
	v_fmac_f32_e32 v34, v22, v22
	v_fmac_f32_e32 v34, v23, v23
	v_fmac_f32_e32 v34, v24, v24
	v_fmac_f32_e32 v34, v25, v25
	v_fmac_f32_e32 v34, v26, v26
	v_fmac_f32_e32 v34, v27, v27
	v_fmac_f32_e32 v34, v28, v28
	v_fmac_f32_e32 v34, v29, v29
	v_fmac_f32_e32 v34, v30, v30
	v_fmac_f32_e32 v34, v31, v31
	v_fmac_f32_e32 v34, v0, v0
	v_fmac_f32_e32 v34, v1, v1
	v_fmac_f32_e32 v34, v2, v2
	v_fmac_f32_e32 v34, v3, v3
	v_fmac_f32_e32 v34, v4, v4
	v_fmac_f32_e32 v34, v5, v5
	v_fmac_f32_e32 v34, v6, v6
	v_fmac_f32_e32 v34, v7, v7
	v_fmac_f32_e32 v34, v8, v8
	v_fmac_f32_e32 v34, v9, v9
	v_fmac_f32_e32 v34, v10, v10
	v_fmac_f32_e32 v34, v11, v11
	v_fmac_f32_e32 v34, v12, v12
	global_store_dwordx2 v[66:67], v[32:33], off offset:112
	v_fmac_f32_e32 v34, v13, v13
	v_pk_mul_f32 v[32:33], v[14:15], v[14:15]
	s_nop 0
	v_add_f32_e32 v32, v32, v34
	v_add_f32_e32 v32, v33, v32
	v_mov_b32_e32 v33, v32
	s_nop 1
	v_permlane32_swap_b32_e32 v32, v33
	v_add_f32_e32 v32, v32, v33
	v_fmamk_f32 v32, v32, 0x3c800000, v241
	v_cmp_gt_f32_e32 vcc, s1, v32
	v_mul_f32_e32 v33, 0x4f800000, v32
	s_nop 0
	v_cndmask_b32_e32 v32, v32, v33, vcc
	v_sqrt_f32_e32 v33, v32
	s_nop 0
	v_add_u32_e32 v34, -1, v33
	v_fma_f32 v35, -v34, v33, v32
	v_cmp_ge_f32_e64 s[2:3], 0, v35
	v_add_u32_e32 v35, 1, v33
	s_nop 0
	v_cndmask_b32_e64 v34, v33, v34, s[2:3]
	v_fma_f32 v33, -v35, v33, v32
	v_cmp_lt_f32_e64 s[2:3], 0, v33
	s_nop 1
	v_cndmask_b32_e64 v33, v34, v35, s[2:3]
	v_mul_f32_e32 v34, 0x37800000, v33
	v_cndmask_b32_e32 v33, v33, v34, vcc
	v_cmp_class_f32_e32 vcc, v32, v240
	s_nop 1
	v_cndmask_b32_e32 v32, v33, v32, vcc
	v_div_scale_f32 v33, s[2:3], v32, v32, 1.0
	v_rcp_f32_e32 v34, v33
	s_nop 0
	v_fma_f32 v35, -v33, v34, 1.0
	v_fmac_f32_e32 v34, v35, v34
	v_div_scale_f32 v35, vcc, 1.0, v32, 1.0
	v_mul_f32_e32 v36, v35, v34
	v_fma_f32 v37, -v33, v36, v35
	v_fmac_f32_e32 v36, v37, v34
	v_fma_f32 v33, -v33, v36, v35
	v_div_fmas_f32 v33, v33, v34, v36
	v_lshlrev_b64 v[34:35], 9, v[40:41]
	v_lshl_add_u64 v[34:35], v[106:107], 0, v[34:35]
	global_load_dwordx2 v[42:43], v[34:35], off
	global_load_dwordx4 v[36:39], v[104:105], off
	v_div_fixup_f32 v32, v33, v32, 1.0
	s_waitcnt vmcnt(1)
	v_lshlrev_b32_e32 v44, 16, v42
	v_mul_f32_e32 v33, 0xbfb8aa3b, v44
	v_exp_f32_e32 v33, v33
	v_and_b32_e32 v45, 0xffff0000, v42
	v_add_f32_e32 v33, 1.0, v33
	v_rcp_f32_e32 v46, v33
	v_pk_mul_f32 v[16:17], v[16:17], v[32:33] op_sel_hi:[1,0]
	v_mul_f32_e32 v33, 0xbfb8aa3b, v45
	v_exp_f32_e32 v33, v33
	s_waitcnt vmcnt(0)
	v_pk_mul_f32 v[16:17], v[36:37], v[16:17]
	v_add_f32_e32 v33, 1.0, v33
	v_rcp_f32_e32 v47, v33
	s_nop 0
	v_pk_mul_f32 v[36:37], v[46:47], v[44:45]
	s_nop 0
	v_pk_mul_f32 v[16:17], v[16:17], v[36:37]
	v_lshlrev_b32_e32 v36, 16, v43
	v_mul_f32_e32 v33, 0xbfb8aa3b, v36
	v_exp_f32_e32 v33, v33
	v_and_b32_e32 v37, 0xffff0000, v43
	v_add_f32_e32 v33, 1.0, v33
	v_rcp_f32_e32 v42, v33
	v_pk_mul_f32 v[18:19], v[18:19], v[32:33] op_sel_hi:[1,0]
	v_mul_f32_e32 v33, 0xbfb8aa3b, v37
	v_exp_f32_e32 v33, v33
	v_pk_mul_f32 v[18:19], v[38:39], v[18:19]
	v_add_f32_e32 v33, 1.0, v33
	v_rcp_f32_e32 v43, v33
	v_pk_mul_f32 v[20:21], v[20:21], v[32:33] op_sel_hi:[1,0]
	v_pk_mul_f32 v[36:37], v[42:43], v[36:37]
	s_nop 0
	v_pk_mul_f32 v[36:37], v[18:19], v[36:37]
	v_cvt_pk_bf16_f32 v18, v16, v17
	v_mad_u64_u32 v[16:17], s[2:3], v40, s83, v[108:109]
	v_cvt_pk_bf16_f32 v19, v36, v37
	v_mad_i32_i24 v17, s15, v227, v17
	global_store_dwordx2 v[16:17], v[18:19], off
	global_load_dwordx2 v[18:19], v[34:35], off offset:16
	s_nop 0
	global_load_dwordx4 v[36:39], v[104:105], off offset:32
	s_waitcnt vmcnt(1)
	v_lshlrev_b32_e32 v40, 16, v18
	v_and_b32_e32 v41, 0xffff0000, v18
	v_mul_f32_e32 v18, 0xbfb8aa3b, v40
	v_exp_f32_e32 v18, v18
	s_waitcnt vmcnt(0)
	v_pk_mul_f32 v[20:21], v[36:37], v[20:21]
	v_add_f32_e32 v18, 1.0, v18
	v_rcp_f32_e32 v42, v18
	v_mul_f32_e32 v18, 0xbfb8aa3b, v41
	v_exp_f32_e32 v18, v18
	s_nop 0
	v_add_f32_e32 v18, 1.0, v18
	v_rcp_f32_e32 v43, v18
	v_lshlrev_b32_e32 v18, 16, v19
	v_mul_f32_e32 v33, 0xbfb8aa3b, v18
	v_exp_f32_e32 v33, v33
	v_pk_mul_f32 v[36:37], v[42:43], v[40:41]
	v_and_b32_e32 v19, 0xffff0000, v19
	v_pk_mul_f32 v[20:21], v[20:21], v[36:37]
	v_add_f32_e32 v33, 1.0, v33
	v_rcp_f32_e32 v36, v33
	v_pk_mul_f32 v[22:23], v[22:23], v[32:33] op_sel_hi:[1,0]
	v_mul_f32_e32 v33, 0xbfb8aa3b, v19
	v_exp_f32_e32 v33, v33
	v_pk_mul_f32 v[22:23], v[38:39], v[22:23]
	v_cvt_pk_bf16_f32 v20, v20, v21
	v_add_f32_e32 v33, 1.0, v33
	v_rcp_f32_e32 v37, v33
	v_pk_mul_f32 v[24:25], v[24:25], v[32:33] op_sel_hi:[1,0]
	v_pk_mul_f32 v[26:27], v[26:27], v[32:33] op_sel_hi:[1,0]
	v_pk_mul_f32 v[28:29], v[28:29], v[32:33] op_sel_hi:[1,0]
	v_pk_mul_f32 v[18:19], v[36:37], v[18:19]
	v_pk_mul_f32 v[0:1], v[0:1], v[32:33] op_sel_hi:[1,0]
	v_pk_mul_f32 v[18:19], v[22:23], v[18:19]
	v_pk_mul_f32 v[2:3], v[2:3], v[32:33] op_sel_hi:[1,0]
	v_cvt_pk_bf16_f32 v21, v18, v19
	global_store_dwordx2 v[16:17], v[20:21], off offset:16
	global_load_dwordx2 v[22:23], v[34:35], off offset:32
	s_nop 0
	global_load_dwordx4 v[18:21], v[104:105], off offset:64
	v_pk_mul_f32 v[4:5], v[4:5], v[32:33] op_sel_hi:[1,0]
	v_pk_mul_f32 v[6:7], v[6:7], v[32:33] op_sel_hi:[1,0]
	v_pk_mul_f32 v[8:9], v[8:9], v[32:33] op_sel_hi:[1,0]
	s_waitcnt vmcnt(1)
	v_lshlrev_b32_e32 v36, 16, v22
	v_and_b32_e32 v37, 0xffff0000, v22
	v_mul_f32_e32 v22, 0xbfb8aa3b, v36
	v_exp_f32_e32 v22, v22
	s_waitcnt vmcnt(0)
	v_pk_mul_f32 v[18:19], v[24:25], v[18:19]
	v_pk_mul_f32 v[20:21], v[26:27], v[20:21]
	v_add_f32_e32 v22, 1.0, v22
	v_rcp_f32_e32 v38, v22
	v_mul_f32_e32 v22, 0xbfb8aa3b, v37
	v_exp_f32_e32 v22, v22
	s_nop 0
	v_add_f32_e32 v22, 1.0, v22
	v_rcp_f32_e32 v39, v22
	v_lshlrev_b32_e32 v22, 16, v23
	v_and_b32_e32 v23, 0xffff0000, v23
	v_pk_mul_f32 v[24:25], v[38:39], v[36:37]
	s_nop 0
	v_pk_mul_f32 v[18:19], v[18:19], v[24:25]
	v_mul_f32_e32 v24, 0xbfb8aa3b, v22
	v_mul_f32_e32 v25, 0xbfb8aa3b, v23
	v_exp_f32_e32 v24, v24
	v_exp_f32_e32 v25, v25
	v_cvt_pk_bf16_f32 v18, v18, v19
	v_add_f32_e32 v24, 1.0, v24
	v_add_f32_e32 v25, 1.0, v25
	v_rcp_f32_e32 v24, v24
	v_rcp_f32_e32 v25, v25
	s_nop 0
	v_pk_mul_f32 v[22:23], v[24:25], v[22:23]
	s_nop 0
	v_pk_mul_f32 v[20:21], v[20:21], v[22:23]
	s_nop 0
	v_cvt_pk_bf16_f32 v19, v20, v21
	global_store_dwordx2 v[16:17], v[18:19], off offset:32
	global_load_dwordx2 v[18:19], v[34:35], off offset:48
	s_nop 0
	global_load_dwordx4 v[20:23], v[104:105], off offset:96
	s_waitcnt vmcnt(1)
	v_lshlrev_b32_e32 v24, 16, v18
	v_and_b32_e32 v25, 0xffff0000, v18
	v_mul_f32_e32 v18, 0xbfb8aa3b, v24
	v_exp_f32_e32 v18, v18
	s_waitcnt vmcnt(0)
	v_pk_mul_f32 v[20:21], v[28:29], v[20:21]
	v_add_f32_e32 v18, 1.0, v18
	v_rcp_f32_e32 v26, v18
	v_mul_f32_e32 v18, 0xbfb8aa3b, v25
	v_exp_f32_e32 v18, v18
	s_nop 0
	v_add_f32_e32 v18, 1.0, v18
	v_rcp_f32_e32 v27, v18
	v_lshlrev_b32_e32 v18, 16, v19
	v_and_b32_e32 v19, 0xffff0000, v19
	v_pk_mul_f32 v[24:25], v[26:27], v[24:25]
	s_nop 0
	v_pk_mul_f32 v[20:21], v[20:21], v[24:25]
	v_mul_f32_e32 v24, 0xbfb8aa3b, v18
	v_mul_f32_e32 v25, 0xbfb8aa3b, v19
	v_exp_f32_e32 v24, v24
	v_exp_f32_e32 v25, v25
	v_pk_mul_f32 v[26:27], v[30:31], v[32:33] op_sel_hi:[1,0]
	v_cvt_pk_bf16_f32 v20, v20, v21
	v_add_f32_e32 v24, 1.0, v24
	v_add_f32_e32 v25, 1.0, v25
	v_rcp_f32_e32 v24, v24
	v_rcp_f32_e32 v25, v25
	v_pk_mul_f32 v[22:23], v[26:27], v[22:23]
	v_pk_mul_f32 v[18:19], v[24:25], v[18:19]
	s_nop 0
	v_pk_mul_f32 v[18:19], v[22:23], v[18:19]
	s_nop 0
	v_cvt_pk_bf16_f32 v21, v18, v19
	global_store_dwordx2 v[16:17], v[20:21], off offset:48
	global_load_dwordx2 v[22:23], v[34:35], off offset:64
	s_nop 0
	global_load_dwordx4 v[18:21], v[104:105], off offset:128
	s_waitcnt vmcnt(1)
	v_lshlrev_b32_e32 v24, 16, v22
	v_and_b32_e32 v25, 0xffff0000, v22
	v_mul_f32_e32 v22, 0xbfb8aa3b, v24
	s_waitcnt vmcnt(0)
	v_pk_mul_f32 v[0:1], v[0:1], v[18:19]
	v_mul_f32_e32 v18, 0xbfb8aa3b, v25
	v_exp_f32_e32 v22, v22
	v_exp_f32_e32 v18, v18
	v_pk_mul_f32 v[2:3], v[2:3], v[20:21]
	v_add_f32_e32 v22, 1.0, v22
	v_add_f32_e32 v18, 1.0, v18
	v_rcp_f32_e32 v26, v22
	v_rcp_f32_e32 v27, v18
	s_nop 0
	v_pk_mul_f32 v[18:19], v[26:27], v[24:25]
	s_nop 0
	v_pk_mul_f32 v[0:1], v[0:1], v[18:19]
	v_lshlrev_b32_e32 v18, 16, v23
	v_and_b32_e32 v19, 0xffff0000, v23
	v_mul_f32_e32 v22, 0xbfb8aa3b, v18
	v_mul_f32_e32 v20, 0xbfb8aa3b, v19
	v_exp_f32_e32 v22, v22
	v_exp_f32_e32 v20, v20
	v_cvt_pk_bf16_f32 v0, v0, v1
	v_add_f32_e32 v22, 1.0, v22
	v_add_f32_e32 v20, 1.0, v20
	v_rcp_f32_e32 v22, v22
	v_rcp_f32_e32 v23, v20
	s_nop 0
	v_pk_mul_f32 v[18:19], v[22:23], v[18:19]
	s_nop 0
	v_pk_mul_f32 v[2:3], v[2:3], v[18:19]
	s_nop 0
	v_cvt_pk_bf16_f32 v1, v2, v3
	global_store_dwordx2 v[16:17], v[0:1], off offset:64
	global_load_dwordx2 v[18:19], v[34:35], off offset:80
	s_nop 0
	global_load_dwordx4 v[0:3], v[104:105], off offset:160
	s_waitcnt vmcnt(1)
	v_lshlrev_b32_e32 v20, 16, v18
	v_and_b32_e32 v21, 0xffff0000, v18
	v_mul_f32_e32 v18, 0xbfb8aa3b, v20
	s_waitcnt vmcnt(0)
	v_pk_mul_f32 v[0:1], v[4:5], v[0:1]
	v_mul_f32_e32 v4, 0xbfb8aa3b, v21
	v_exp_f32_e32 v18, v18
	v_exp_f32_e32 v4, v4
	v_pk_mul_f32 v[2:3], v[6:7], v[2:3]
	v_add_f32_e32 v18, 1.0, v18
	v_add_f32_e32 v4, 1.0, v4
	v_rcp_f32_e32 v22, v18
	v_rcp_f32_e32 v23, v4
	s_nop 0
	v_pk_mul_f32 v[4:5], v[22:23], v[20:21]
	s_nop 0
	v_pk_mul_f32 v[0:1], v[0:1], v[4:5]
	v_lshlrev_b32_e32 v4, 16, v19
	v_and_b32_e32 v5, 0xffff0000, v19
	v_mul_f32_e32 v18, 0xbfb8aa3b, v4
	v_mul_f32_e32 v6, 0xbfb8aa3b, v5
	v_exp_f32_e32 v18, v18
	v_exp_f32_e32 v6, v6
	v_cvt_pk_bf16_f32 v0, v0, v1
	v_add_f32_e32 v18, 1.0, v18
	v_add_f32_e32 v6, 1.0, v6
	v_rcp_f32_e32 v18, v18
	v_rcp_f32_e32 v19, v6
	s_nop 0
	v_pk_mul_f32 v[4:5], v[18:19], v[4:5]
	s_nop 0
	v_pk_mul_f32 v[2:3], v[2:3], v[4:5]
	s_nop 0
	v_cvt_pk_bf16_f32 v1, v2, v3
	global_store_dwordx2 v[16:17], v[0:1], off offset:80
	global_load_dwordx2 v[4:5], v[34:35], off offset:96
	s_nop 0
	global_load_dwordx4 v[0:3], v[104:105], off offset:192
	s_waitcnt vmcnt(1)
	v_lshlrev_b32_e32 v6, 16, v4
	v_and_b32_e32 v7, 0xffff0000, v4
	v_mul_f32_e32 v4, 0xbfb8aa3b, v6
	v_exp_f32_e32 v4, v4
	s_waitcnt vmcnt(0)
	v_pk_mul_f32 v[0:1], v[8:9], v[0:1]
	v_pk_mul_f32 v[8:9], v[10:11], v[32:33] op_sel_hi:[1,0]
	v_pk_mul_f32 v[10:11], v[12:13], v[32:33] op_sel_hi:[1,0]
	v_add_f32_e32 v4, 1.0, v4
	v_rcp_f32_e32 v18, v4
	v_mul_f32_e32 v4, 0xbfb8aa3b, v7
	v_exp_f32_e32 v4, v4
	v_pk_mul_f32 v[2:3], v[8:9], v[2:3]
	v_add_f32_e32 v4, 1.0, v4
	v_rcp_f32_e32 v19, v4
	v_lshlrev_b32_e32 v4, 16, v5
	v_and_b32_e32 v5, 0xffff0000, v5
	v_pk_mul_f32 v[6:7], v[18:19], v[6:7]
	s_nop 0
	v_pk_mul_f32 v[0:1], v[0:1], v[6:7]
	v_mul_f32_e32 v6, 0xbfb8aa3b, v4
	v_mul_f32_e32 v7, 0xbfb8aa3b, v5
	v_exp_f32_e32 v6, v6
	v_exp_f32_e32 v7, v7
	v_cvt_pk_bf16_f32 v0, v0, v1
	v_add_f32_e32 v6, 1.0, v6
	v_add_f32_e32 v7, 1.0, v7
	v_rcp_f32_e32 v6, v6
	v_rcp_f32_e32 v7, v7
	s_nop 0
	v_pk_mul_f32 v[4:5], v[6:7], v[4:5]
	s_nop 0
	v_pk_mul_f32 v[2:3], v[2:3], v[4:5]
	s_nop 0
	v_cvt_pk_bf16_f32 v1, v2, v3
	global_store_dwordx2 v[16:17], v[0:1], off offset:96
	global_load_dwordx2 v[0:1], v[34:35], off offset:112
	s_nop 0
	global_load_dwordx4 v[2:5], v[104:105], off offset:224
	s_waitcnt vmcnt(1)
	v_lshlrev_b32_e32 v6, 16, v0
	v_and_b32_e32 v7, 0xffff0000, v0
	v_mul_f32_e32 v0, 0xbfb8aa3b, v6
	v_exp_f32_e32 v0, v0
	s_waitcnt vmcnt(0)
	v_pk_mul_f32 v[2:3], v[10:11], v[2:3]
	v_add_f32_e32 v0, 1.0, v0
	v_rcp_f32_e32 v8, v0
	v_mul_f32_e32 v0, 0xbfb8aa3b, v7
	v_exp_f32_e32 v0, v0
	s_nop 0
	v_add_f32_e32 v0, 1.0, v0
	v_rcp_f32_e32 v9, v0
	v_lshlrev_b32_e32 v0, 16, v1
	v_and_b32_e32 v1, 0xffff0000, v1
	v_pk_mul_f32 v[6:7], v[8:9], v[6:7]
	s_nop 0
	v_pk_mul_f32 v[2:3], v[2:3], v[6:7]
	v_mul_f32_e32 v6, 0xbfb8aa3b, v0
	v_mul_f32_e32 v7, 0xbfb8aa3b, v1
	v_exp_f32_e32 v6, v6
	v_exp_f32_e32 v7, v7
	v_pk_mul_f32 v[8:9], v[14:15], v[32:33] op_sel_hi:[1,0]
	v_cvt_pk_bf16_f32 v2, v2, v3
	v_add_f32_e32 v6, 1.0, v6
	v_add_f32_e32 v7, 1.0, v7
	v_rcp_f32_e32 v6, v6
	v_rcp_f32_e32 v7, v7
	v_pk_mul_f32 v[4:5], v[8:9], v[4:5]
	v_pk_mul_f32 v[0:1], v[6:7], v[0:1]
	s_nop 0
	v_pk_mul_f32 v[0:1], v[4:5], v[0:1]
	s_nop 0
	v_cvt_pk_bf16_f32 v3, v0, v1
	global_store_dwordx2 v[16:17], v[2:3], off offset:112
	s_waitcnt lgkmcnt(0)
	s_cbranch_scc0 .LBB0_768
	v_readlane_b32 s75, v254, 28
	s_mov_b32 s76, s18
	v_readlane_b32 s79, v254, 33
	s_mov_b64 s[46:47], s[20:21]
	v_readlane_b32 s44, v254, 38
